# dead-row MFMA elision: in partial 256-row expert tiles, waves 4-7 skip the MFMAs of 16-row blocks that hold no rows (rows<=192: blocks 4-7, rows<=224: blocks 6-7)
# baseline (speedup 1.0000x reference)
; #define G_DMA_A(buf, t, i_) __builtin_amdgcn_raw_ptr_buffer_load_lds(ra, (LAS void*)(lds + (buf) * 65536 + a_wu + (i_) * 8192), 16, ao##i_, (unsigned)(t) * 128u, 0, 0)
; #define G_ISSUE_B(t) do { const unsigned so_ = (unsigned)(t) * 64u * ldbB; _Pragma("unroll") for (int i_ = 0; i_ < 8; ++i_) sb[i_] = __builtin_bit_cast(f32x4, __builtin_amdgcn_raw_buffer_load_b128(rb, bo, so_ + (unsigned)i_ * ldbB, 0)); } while (0)
; #define G_RETIRE() asm volatile("s_waitcnt vmcnt(0)" : "+v"(sb[0]), "+v"(sb[1]), "+v"(sb[2]), "+v"(sb[3]), "+v"(sb[4]), "+v"(sb[5]), "+v"(sb[6]), "+v"(sb[7]) :: "memory")
; #define G_WRITE_B(buf) do { LAS unsigned char* d_ = lds + (buf) * 65536; \
;         _Pragma("unroll") for (int j_ = 0; j_ < 4; ++j_) { u32x4 w_; w_.x = cvtpk(sb[0][j_], sb[1][j_]); w_.y = cvtpk(sb[2][j_], sb[3][j_]); w_.z = cvtpk(sb[4][j_], sb[5][j_]); w_.w = cvtpk(sb[6][j_], sb[7][j_]); \
;             *(LAS u32x4*)(d_ + 32768 + T.b_w + ((T.b_rot + 64u * j_) & 255u)) = w_; } } while (0)
; #define G_BAR() do { asm volatile("s_waitcnt lgkmcnt(0)" ::: "memory"); __builtin_amdgcn_s_barrier(); asm volatile("" ::: "memory"); } while (0)
; #define G_DMA_A(buf, t, i_) __builtin_amdgcn_raw_ptr_buffer_load_lds(ra, (LAS void*)(lds + (buf) * 65536 + a_wu + (i_) * 8192), 16, ao##i_, (unsigned)(t) * 128u, 0, 0)
; #define G_ISSUE_B(t) do { const unsigned so_ = (unsigned)(t) * 64u * ldbB; _Pragma("unroll") for (int i_ = 0; i_ < 8; ++i_) sb[i_] = __builtin_bit_cast(f32x4, __builtin_amdgcn_raw_buffer_load_b128(rb, bo, so_ + (unsigned)i_ * ldbB, 0)); } while (0)
; #define G_RETIRE() asm volatile("s_waitcnt vmcnt(0)" : "+v"(sb[0]), "+v"(sb[1]), "+v"(sb[2]), "+v"(sb[3]), "+v"(sb[4]), "+v"(sb[5]), "+v"(sb[6]), "+v"(sb[7]) :: "memory")
; __device__ __forceinline__ void gemm_kloop(f32x4 (&acc)[8][4], LAS unsigned char* lds, const GemmT& T, ...
;     ...
;     G_ISSUE_B(0); G_DMA_A(0, 0, 0); G_DMA_A(0, 0, 1); G_DMA_A(0, 0, 2); G_DMA_A(0, 0, 3); G_RETIRE(); G_WRITE_B(0);
;     if (nt > 1) G_ISSUE_B(1);
;     G_BAR();
; __device__ __forceinline__ void acc_zero(f32x4 (&acc)[8][4]) {
; #pragma unroll
;     for (int m = 0; m < 8; ++m)
; #pragma unroll
;         for (int n = 0; n < 4; ++n) acc[m][n] = (f32x4){0.f, 0.f, 0.f, 0.f};
.LBB0_1263:
	s_cbranch_execz .LBB0_1267
	s_sub_i32 s98, s87, s2
	s_sub_i32 s98, s98, 0x81
	s_lshr_b32 s98, s98, 5
	s_sub_i32 s98, s98, 1
	s_max_i32 s98, s98, 0
	s_min_i32 s98, s98, 2
	s_cmp_eq_u32 s1, 0
	s_cselect_b32 s98, 2, s98
	v_readfirstlane_b32 s1, v229
	s_and_b32 s1, s1, 0xfffffc00
	s_add_i32 s1, s1, 0
	s_mov_b32 s38, s26
	s_mov_b32 s39, s27
	s_mov_b32 m0, s1
	v_add_u32_e32 v3, v227, v218
	buffer_load_dwordx4 v223, s[36:39], 0 offen lds
	s_add_i32 m0, s1, 0x2000
	v_mov_b32_e32 v36, 0
	buffer_load_dwordx4 v222, s[36:39], 0 offen lds
	s_add_i32 m0, s1, 0x4000
	s_mov_b32 s3, 0
	buffer_load_dwordx4 v221, s[36:39], 0 offen lds
	s_add_i32 m0, s1, 0x6000
	s_mov_b32 s4, 0x10e000
	buffer_load_dwordx4 v224, s[36:39], 0 offen lds
	s_waitcnt vmcnt(4)
	s_waitcnt vmcnt(0)
	s_movk_i32 s5, 0x80
	v_cvt_pk_bf16_f32 v4, v114, v126
	v_cvt_pk_bf16_f32 v5, v130, v118
	v_cvt_pk_bf16_f32 v6, v122, v134
	v_cvt_pk_bf16_f32 v7, v142, v146
	ds_write_b128 v228, v[4:7] offset:32768
	v_cvt_pk_bf16_f32 v4, v115, v127
	v_cvt_pk_bf16_f32 v5, v131, v119
	v_cvt_pk_bf16_f32 v6, v123, v135
	v_cvt_pk_bf16_f32 v7, v143, v147
	ds_write_b128 v228, v[4:7] offset:32832
	v_cvt_pk_bf16_f32 v4, v116, v128
	v_cvt_pk_bf16_f32 v5, v132, v120
	v_cvt_pk_bf16_f32 v6, v124, v136
	v_cvt_pk_bf16_f32 v7, v144, v148
	ds_write_b128 v228, v[4:7] offset:32896
	v_cvt_pk_bf16_f32 v4, v117, v129
	v_cvt_pk_bf16_f32 v5, v133, v121
	v_cvt_pk_bf16_f32 v6, v125, v137
	v_cvt_pk_bf16_f32 v7, v145, v149
	ds_write_b128 v3, v[4:7] offset:32768
	buffer_load_dwordx4 v[4:7], v225, s[24:27], s67 offen
	buffer_load_dwordx4 v[8:11], v225, s[24:27], s76 offen
	buffer_load_dwordx4 v[12:15], v225, s[24:27], s77 offen
	buffer_load_dwordx4 v[16:19], v225, s[24:27], s78 offen
	buffer_load_dwordx4 v[20:23], v225, s[24:27], s79 offen
	buffer_load_dwordx4 v[28:31], v225, s[24:27], s80 offen
	buffer_load_dwordx4 v[24:27], v225, s[24:27], s81 offen
	buffer_load_dwordx4 v[32:35], v225, s[24:27], s82 offen
	s_waitcnt lgkmcnt(0)
	s_barrier
	v_mov_b32_e32 v37, v36
	v_mov_b32_e32 v38, v36
	v_mov_b32_e32 v39, v36
	v_mov_b32_e32 v40, v36
	v_mov_b32_e32 v41, v36
	v_mov_b32_e32 v42, v36
	v_mov_b32_e32 v43, v36
	v_mov_b32_e32 v44, v36
	v_mov_b32_e32 v45, v36
	v_mov_b32_e32 v46, v36
	v_mov_b32_e32 v47, v36
	v_mov_b32_e32 v48, v36
	v_mov_b32_e32 v49, v36
	v_mov_b32_e32 v50, v36
	v_mov_b32_e32 v51, v36
	v_mov_b32_e32 v52, v36
	v_mov_b32_e32 v53, v36
	v_mov_b32_e32 v54, v36
	v_mov_b32_e32 v55, v36
	v_mov_b32_e32 v56, v36
	v_mov_b32_e32 v57, v36
	v_mov_b32_e32 v58, v36
	v_mov_b32_e32 v59, v36
	v_mov_b32_e32 v60, v36
	v_mov_b32_e32 v61, v36
	v_mov_b32_e32 v62, v36
	v_mov_b32_e32 v63, v36
	v_mov_b32_e32 v64, v36
	v_mov_b32_e32 v65, v36
	v_mov_b32_e32 v66, v36
	v_mov_b32_e32 v67, v36
	v_mov_b32_e32 v68, v36
	v_mov_b32_e32 v69, v36
	v_mov_b32_e32 v70, v36
	v_mov_b32_e32 v71, v36
	v_mov_b32_e32 v72, v36
	v_mov_b32_e32 v73, v36
	v_mov_b32_e32 v74, v36
	v_mov_b32_e32 v75, v36
	v_mov_b32_e32 v76, v36
	v_mov_b32_e32 v77, v36
	v_mov_b32_e32 v78, v36
	v_mov_b32_e32 v79, v36
	v_mov_b32_e32 v80, v36
	v_mov_b32_e32 v81, v36
	v_mov_b32_e32 v82, v36
	v_mov_b32_e32 v83, v36
	v_mov_b32_e32 v84, v36
	v_mov_b32_e32 v85, v36
	v_mov_b32_e32 v86, v36
	v_mov_b32_e32 v87, v36
	v_mov_b32_e32 v88, v36
	v_mov_b32_e32 v89, v36
	v_mov_b32_e32 v90, v36
	v_mov_b32_e32 v91, v36
	v_mov_b32_e32 v92, v36
	v_mov_b32_e32 v93, v36
	v_mov_b32_e32 v94, v36
	v_mov_b32_e32 v95, v36
	v_mov_b32_e32 v96, v36
	v_mov_b32_e32 v97, v36
	v_mov_b32_e32 v98, v36
	v_mov_b32_e32 v99, v36
	v_mov_b32_e32 v100, v36
	v_mov_b32_e32 v101, v36
	v_mov_b32_e32 v102, v36
	v_mov_b32_e32 v103, v36
	v_mov_b32_e32 v104, v36
	v_mov_b32_e32 v105, v36
	v_mov_b32_e32 v106, v36
	v_mov_b32_e32 v107, v36
	v_mov_b32_e32 v108, v36
	v_mov_b32_e32 v109, v36
	v_mov_b32_e32 v110, v36
	v_mov_b32_e32 v111, v36
	v_mov_b32_e32 v112, v36
	v_mov_b32_e32 v113, v36
	v_mov_b32_e32 v114, v36
	v_mov_b32_e32 v115, v36
	v_mov_b32_e32 v116, v36
	v_mov_b32_e32 v117, v36
	v_mov_b32_e32 v118, v36
	v_mov_b32_e32 v119, v36
	v_mov_b32_e32 v120, v36
	v_mov_b32_e32 v121, v36
	v_mov_b32_e32 v122, v36
	v_mov_b32_e32 v123, v36
	v_mov_b32_e32 v124, v36
	v_mov_b32_e32 v125, v36
	v_mov_b32_e32 v126, v36
	v_mov_b32_e32 v127, v36
	v_mov_b32_e32 v128, v36
	v_mov_b32_e32 v129, v36
	v_mov_b32_e32 v130, v36
	v_mov_b32_e32 v131, v36
	v_mov_b32_e32 v132, v36
	v_mov_b32_e32 v133, v36
	v_mov_b32_e32 v134, v36
	v_mov_b32_e32 v135, v36
	v_mov_b32_e32 v136, v36
	v_mov_b32_e32 v137, v36
	v_mov_b32_e32 v138, v36
	v_mov_b32_e32 v139, v36
	v_mov_b32_e32 v140, v36
	v_mov_b32_e32 v141, v36
	v_mov_b32_e32 v142, v36
	v_mov_b32_e32 v143, v36
	v_mov_b32_e32 v144, v36
	v_mov_b32_e32 v145, v36
	v_mov_b32_e32 v146, v36
	v_mov_b32_e32 v147, v36
	v_mov_b32_e32 v148, v36
	v_mov_b32_e32 v149, v36
	v_mov_b32_e32 v150, v36
	v_mov_b32_e32 v151, v36
	v_mov_b32_e32 v152, v36
	v_mov_b32_e32 v153, v36
	v_mov_b32_e32 v154, v36
	v_mov_b32_e32 v155, v36
	v_mov_b32_e32 v156, v36
	v_mov_b32_e32 v157, v36
	v_mov_b32_e32 v158, v36
	v_mov_b32_e32 v159, v36
	v_mov_b32_e32 v160, v36
	v_mov_b32_e32 v161, v36
	v_mov_b32_e32 v162, v36
	v_mov_b32_e32 v163, v36
; #define G_DMA_A(buf, t, i_) __builtin_amdgcn_raw_ptr_buffer_load_lds(ra, (LAS void*)(lds + (buf) * 65536 + a_wu + (i_) * 8192), 16, ao##i_, (unsigned)(t) * 128u, 0, 0)
; #define G_ISSUE_B(t) do { const unsigned so_ = (unsigned)(t) * 64u * ldbB; _Pragma("unroll") for (int i_ = 0; i_ < 8; ++i_) sb[i_] = __builtin_bit_cast(f32x4, __builtin_amdgcn_raw_buffer_load_b128(rb, bo, so_ + (unsigned)i_ * ldbB, 0)); } while (0)
; #define G_RETIRE() asm volatile("s_waitcnt vmcnt(0)" : "+v"(sb[0]), "+v"(sb[1]), "+v"(sb[2]), "+v"(sb[3]), "+v"(sb[4]), "+v"(sb[5]), "+v"(sb[6]), "+v"(sb[7]) :: "memory")
; #define G_WRITE_B(buf) do { LAS unsigned char* d_ = lds + (buf) * 65536; \
;         _Pragma("unroll") for (int j_ = 0; j_ < 4; ++j_) { u32x4 w_; w_.x = cvtpk(sb[0][j_], sb[1][j_]); w_.y = cvtpk(sb[2][j_], sb[3][j_]); w_.z = cvtpk(sb[4][j_], sb[5][j_]); w_.w = cvtpk(sb[6][j_], sb[7][j_]); \
;             *(LAS u32x4*)(d_ + 32768 + T.b_w + ((T.b_rot + 64u * j_) & 255u)) = w_; } } while (0)
; #define G_LDB(dst, buf, ks) do { const LAS unsigned char* s_ = lds + (buf) * 65536 + (ks) * 1024; _Pragma("unroll") for (int n_ = 0; n_ < 4; ++n_) dst[n_] = *(const LAS bf16x8*)(s_ + T.b_r + n_ * 2048); } while (0)
; #define G_LDA(dst, buf, ks, h_) do { const LAS unsigned char* s_ = lds + (buf) * 65536 + (ks) * 1024; _Pragma("unroll") for (int m_ = 0; m_ < 4; ++m_) dst[m_] = *(const LAS bf16x8*)(s_ + T.a_r + ((h_) * 4 + m_) * 2048); } while (0)
; #define G_SB() __builtin_amdgcn_sched_barrier(0)
; #define G_DMA_A(buf, t, i_) __builtin_amdgcn_raw_ptr_buffer_load_lds(ra, (LAS void*)(lds + (buf) * 65536 + a_wu + (i_) * 8192), 16, ao##i_, (unsigned)(t) * 128u, 0, 0)
; __device__ __forceinline__ void gemm_kloop(f32x4 (&acc)[8][4], LAS unsigned char* lds, const GemmT& T, ...
;     ...
;     for (int t = 0; t < nt; ++t) { const int cur = t & 1; const bool w1 = t + 1 < nt, i2 = t + 2 < nt;
;         G_LDB(Bf0, cur, 0); G_LDA(AtA, cur, 0, 0); G_SB();
;         G_LDA(AtB, cur, 0, 1); if (w1) { G_DMA_A(cur ^ 1, t + 1, 0); G_DMA_A(cur ^ 1, t + 1, 1); G_DMA_A(cur ^ 1, t + 1, 2); G_DMA_A(cur ^ 1, t + 1, 3); } G_MMA(AtA, Bf0, 0); G_SB();
;         G_LDB(Bf1, cur, 1); G_LDA(AtA, cur, 1, 0); G_MMA(AtB, Bf0, 1); G_SB();
;         G_LDA(AtB, cur, 1, 1); if (w1) { G_RETIRE(); G_WRITE_B(cur ^ 1); } if (i2) G_ISSUE_B(t + 2); G_MMA(AtA, Bf1, 0); G_SB();
;         G_MMA(AtB, Bf1, 1); G_SB();
.LBB0_1265:
	s_and_b32 s6, s3, 0x10000
	s_add_i32 s7, s6, 0
	v_add_u32_e32 v3, s7, v226
	v_add_u32_e32 v208, s7, v216
	ds_read_b128 v[164:167], v3 offset:32768
	ds_read_b128 v[168:171], v3 offset:34816
	ds_read_b128 v[172:175], v3 offset:36864
	ds_read_b128 v[176:179], v3 offset:38912
	ds_read_b128 v[180:183], v208
	ds_read_b128 v[184:187], v208 offset:2048
	ds_read_b128 v[188:191], v208 offset:4096
	ds_read_b128 v[192:195], v208 offset:6144
	s_xor_b32 s6, s6, 0x10000
	s_add_i32 s7, s1, s6
	s_add_i32 s10, s7, 0x2000
	s_mov_b32 m0, s7
	s_waitcnt lgkmcnt(3)
	v_mfma_f32_16x16x32_bf16 v[160:163], v[164:167], v[180:183], v[160:163]
	s_add_i32 s9, s7, 0x4000
	s_add_i32 s8, s7, 0x6000
	v_mfma_f32_16x16x32_bf16 v[156:159], v[168:171], v[180:183], v[156:159]
	v_mfma_f32_16x16x32_bf16 v[152:155], v[172:175], v[180:183], v[152:155]
	v_mfma_f32_16x16x32_bf16 v[148:151], v[176:179], v[180:183], v[148:151]
	s_waitcnt lgkmcnt(2)
	v_mfma_f32_16x16x32_bf16 v[144:147], v[164:167], v[184:187], v[144:147]
	v_mfma_f32_16x16x32_bf16 v[140:143], v[168:171], v[184:187], v[140:143]
	v_mfma_f32_16x16x32_bf16 v[136:139], v[172:175], v[184:187], v[136:139]
	v_mfma_f32_16x16x32_bf16 v[132:135], v[176:179], v[184:187], v[132:135]
	ds_read_b128 v[180:183], v208 offset:8192
	ds_read_b128 v[184:187], v208 offset:10240
	ds_read_b128 v[196:199], v208 offset:12288
	ds_read_b128 v[200:203], v208 offset:14336
	buffer_load_dwordx4 v223, s[36:39], s5 offen lds
	s_mov_b32 m0, s10
	s_waitcnt lgkmcnt(5)
	v_mfma_f32_16x16x32_bf16 v[128:131], v[164:167], v[188:191], v[128:131]
	buffer_load_dwordx4 v222, s[36:39], s5 offen lds
	s_mov_b32 m0, s9
	s_nop 0
	buffer_load_dwordx4 v221, s[36:39], s5 offen lds
	s_mov_b32 m0, s8
	v_mfma_f32_16x16x32_bf16 v[124:127], v[168:171], v[188:191], v[124:127]
	buffer_load_dwordx4 v224, s[36:39], s5 offen lds
	v_mfma_f32_16x16x32_bf16 v[120:123], v[172:175], v[188:191], v[120:123]
	v_mfma_f32_16x16x32_bf16 v[116:119], v[176:179], v[188:191], v[116:119]
	s_waitcnt lgkmcnt(4)
	v_mfma_f32_16x16x32_bf16 v[112:115], v[164:167], v[192:195], v[112:115]
	v_mfma_f32_16x16x32_bf16 v[108:111], v[168:171], v[192:195], v[108:111]
	v_mfma_f32_16x16x32_bf16 v[104:107], v[172:175], v[192:195], v[104:107]
	v_mfma_f32_16x16x32_bf16 v[100:103], v[176:179], v[192:195], v[100:103]
	s_cmp_eq_u32 s98, 0
	s_cbranch_scc1 .Lmy_elga
	s_waitcnt lgkmcnt(3)
	v_mfma_f32_16x16x32_bf16 v[96:99], v[164:167], v[180:183], v[96:99]
	v_mfma_f32_16x16x32_bf16 v[92:95], v[168:171], v[180:183], v[92:95]
	v_mfma_f32_16x16x32_bf16 v[88:91], v[172:175], v[180:183], v[88:91]
	v_mfma_f32_16x16x32_bf16 v[84:87], v[176:179], v[180:183], v[84:87]
	s_waitcnt lgkmcnt(2)
	v_mfma_f32_16x16x32_bf16 v[80:83], v[164:167], v[184:187], v[80:83]
	v_mfma_f32_16x16x32_bf16 v[76:79], v[168:171], v[184:187], v[76:79]
	v_mfma_f32_16x16x32_bf16 v[72:75], v[172:175], v[184:187], v[72:75]
	v_mfma_f32_16x16x32_bf16 v[68:71], v[176:179], v[184:187], v[68:71]
	s_cmp_lt_u32 s98, 2
	s_cbranch_scc1 .Lmy_elga
	s_waitcnt lgkmcnt(1)
	v_mfma_f32_16x16x32_bf16 v[64:67], v[164:167], v[196:199], v[64:67]
	v_mfma_f32_16x16x32_bf16 v[60:63], v[168:171], v[196:199], v[60:63]
	v_mfma_f32_16x16x32_bf16 v[56:59], v[172:175], v[196:199], v[56:59]
	v_mfma_f32_16x16x32_bf16 v[52:55], v[176:179], v[196:199], v[52:55]
	s_waitcnt lgkmcnt(0)
	v_mfma_f32_16x16x32_bf16 v[48:51], v[164:167], v[200:203], v[48:51]
	v_mfma_f32_16x16x32_bf16 v[44:47], v[168:171], v[200:203], v[44:47]
.Lmy_elga:
	ds_read_b128 v[164:167], v3 offset:33792
	ds_read_b128 v[168:171], v3 offset:35840
	ds_read_b128 v[180:183], v3 offset:37888
	ds_read_b128 v[184:187], v3 offset:39936
	s_cmp_lt_u32 s98, 2
	s_cbranch_scc1 .Lmy_elgb
	v_mfma_f32_16x16x32_bf16 v[40:43], v[172:175], v[200:203], v[40:43]
.Lmy_elgb:
	ds_read_b128 v[172:175], v208 offset:9216
	ds_read_b128 v[188:191], v208 offset:11264
	ds_read_b128 v[192:195], v208 offset:13312
	ds_read_b128 v[196:199], v208 offset:15360
	s_cmp_lt_u32 s98, 2
	s_cbranch_scc1 .Lmy_elgd
	v_mfma_f32_16x16x32_bf16 v[36:39], v[176:179], v[200:203], v[36:39]
.Lmy_elgd:
	ds_read_b128 v[176:179], v208 offset:1024
	ds_read_b128 v[200:203], v208 offset:3072
	ds_read_b128 v[204:207], v208 offset:5120
	ds_read_b128 v[208:211], v208 offset:7168
	s_cmp_eq_u32 s98, 0
	s_cbranch_scc1 .Lmy_elgc
	s_waitcnt lgkmcnt(7)
	v_mfma_f32_16x16x32_bf16 v[96:99], v[164:167], v[172:175], v[96:99]
	v_mfma_f32_16x16x32_bf16 v[92:95], v[168:171], v[172:175], v[92:95]
	v_mfma_f32_16x16x32_bf16 v[88:91], v[180:183], v[172:175], v[88:91]
	v_mfma_f32_16x16x32_bf16 v[84:87], v[184:187], v[172:175], v[84:87]
	s_waitcnt lgkmcnt(6)
	v_mfma_f32_16x16x32_bf16 v[80:83], v[164:167], v[188:191], v[80:83]
	v_mfma_f32_16x16x32_bf16 v[76:79], v[168:171], v[188:191], v[76:79]
	v_mfma_f32_16x16x32_bf16 v[72:75], v[180:183], v[188:191], v[72:75]
	v_mfma_f32_16x16x32_bf16 v[68:71], v[184:187], v[188:191], v[68:71]
	s_cmp_lt_u32 s98, 2
	s_cbranch_scc1 .Lmy_elgc
	s_waitcnt lgkmcnt(5)
	v_mfma_f32_16x16x32_bf16 v[64:67], v[164:167], v[192:195], v[64:67]
	v_mfma_f32_16x16x32_bf16 v[60:63], v[168:171], v[192:195], v[60:63]
	v_mfma_f32_16x16x32_bf16 v[56:59], v[180:183], v[192:195], v[56:59]
	v_mfma_f32_16x16x32_bf16 v[52:55], v[184:187], v[192:195], v[52:55]
	s_waitcnt lgkmcnt(4)
	v_mfma_f32_16x16x32_bf16 v[48:51], v[164:167], v[196:199], v[48:51]
	v_mfma_f32_16x16x32_bf16 v[44:47], v[168:171], v[196:199], v[44:47]
	v_mfma_f32_16x16x32_bf16 v[40:43], v[180:183], v[196:199], v[40:43]
	v_mfma_f32_16x16x32_bf16 v[36:39], v[184:187], v[196:199], v[36:39]
; #define G_DMA_A(buf, t, i_) __builtin_amdgcn_raw_ptr_buffer_load_lds(ra, (LAS void*)(lds + (buf) * 65536 + a_wu + (i_) * 8192), 16, ao##i_, (unsigned)(t) * 128u, 0, 0)
; #define G_ISSUE_B(t) do { const unsigned so_ = (unsigned)(t) * 64u * ldbB; _Pragma("unroll") for (int i_ = 0; i_ < 8; ++i_) sb[i_] = __builtin_bit_cast(f32x4, __builtin_amdgcn_raw_buffer_load_b128(rb, bo, so_ + (unsigned)i_ * ldbB, 0)); } while (0)
; #define G_RETIRE() asm volatile("s_waitcnt vmcnt(0)" : "+v"(sb[0]), "+v"(sb[1]), "+v"(sb[2]), "+v"(sb[3]), "+v"(sb[4]), "+v"(sb[5]), "+v"(sb[6]), "+v"(sb[7]) :: "memory")
; #define G_WRITE_B(buf) do { LAS unsigned char* d_ = lds + (buf) * 65536; \
;         _Pragma("unroll") for (int j_ = 0; j_ < 4; ++j_) { u32x4 w_; w_.x = cvtpk(sb[0][j_], sb[1][j_]); w_.y = cvtpk(sb[2][j_], sb[3][j_]); w_.z = cvtpk(sb[4][j_], sb[5][j_]); w_.w = cvtpk(sb[6][j_], sb[7][j_]); \
;             *(LAS u32x4*)(d_ + 32768 + T.b_w + ((T.b_rot + 64u * j_) & 255u)) = w_; } } while (0)
; #define G_LDB(dst, buf, ks) do { const LAS unsigned char* s_ = lds + (buf) * 65536 + (ks) * 1024; _Pragma("unroll") for (int n_ = 0; n_ < 4; ++n_) dst[n_] = *(const LAS bf16x8*)(s_ + T.b_r + n_ * 2048); } while (0)
; #define G_LDA(dst, buf, ks, h_) do { const LAS unsigned char* s_ = lds + (buf) * 65536 + (ks) * 1024; _Pragma("unroll") for (int m_ = 0; m_ < 4; ++m_) dst[m_] = *(const LAS bf16x8*)(s_ + T.a_r + ((h_) * 4 + m_) * 2048); } while (0)
; #define G_SB() __builtin_amdgcn_sched_barrier(0)
; #define G_BAR() do { asm volatile("s_waitcnt lgkmcnt(0)" ::: "memory"); __builtin_amdgcn_s_barrier(); asm volatile("" ::: "memory"); } while (0)
; __device__ __forceinline__ void gemm_kloop(f32x4 (&acc)[8][4], LAS unsigned char* lds, const GemmT& T, ...
;     ...
;     for (int t = 0; t < nt; ++t) { const int cur = t & 1; const bool w1 = t + 1 < nt, i2 = t + 2 < nt;
;         G_LDB(Bf0, cur, 0); G_LDA(AtA, cur, 0, 0); G_SB();
;         G_LDA(AtB, cur, 0, 1); if (w1) { G_DMA_A(cur ^ 1, t + 1, 0); G_DMA_A(cur ^ 1, t + 1, 1); G_DMA_A(cur ^ 1, t + 1, 2); G_DMA_A(cur ^ 1, t + 1, 3); } G_MMA(AtA, Bf0, 0); G_SB();
;         G_LDB(Bf1, cur, 1); G_LDA(AtA, cur, 1, 0); G_MMA(AtB, Bf0, 1); G_SB();
;         G_LDA(AtB, cur, 1, 1); if (w1) { G_RETIRE(); G_WRITE_B(cur ^ 1); } if (i2) G_ISSUE_B(t + 2); G_MMA(AtA, Bf1, 0); G_SB();
;         G_MMA(AtB, Bf1, 1); G_SB();
;         G_BAR(); }
.Lmy_elgc:
	s_waitcnt vmcnt(0)
	s_add_i32 s7, s4, 0xffff2000
	s_waitcnt lgkmcnt(3)
	v_mfma_f32_16x16x32_bf16 v[160:163], v[164:167], v[176:179], v[160:163]
	v_cvt_pk_bf16_f32 v228, v5, v9
	v_cvt_pk_bf16_f32 v232, v6, v10
	s_add_i32 s8, s4, 0xffff4000
	v_mfma_f32_16x16x32_bf16 v[156:159], v[168:171], v[176:179], v[156:159]
	v_cvt_pk_bf16_f32 v229, v13, v17
	v_cvt_pk_bf16_f32 v233, v14, v18
	v_cvt_pk_bf16_f32 v230, v21, v29
	v_mfma_f32_16x16x32_bf16 v[152:155], v[180:183], v[176:179], v[152:155]
	v_cvt_pk_bf16_f32 v234, v22, v30
	v_cvt_pk_bf16_f32 v231, v25, v33
	v_cvt_pk_bf16_f32 v235, v26, v34
	v_mfma_f32_16x16x32_bf16 v[148:151], v[184:187], v[176:179], v[148:151]
	v_cvt_pk_bf16_f32 v172, v4, v8
	v_cvt_pk_bf16_f32 v173, v12, v16
	v_cvt_pk_bf16_f32 v174, v20, v28
	s_waitcnt lgkmcnt(2)
	v_mfma_f32_16x16x32_bf16 v[144:147], v[164:167], v[200:203], v[144:147]
	v_cvt_pk_bf16_f32 v175, v24, v32
	v_add_u32_e32 v3, s6, v227
	v_mfma_f32_16x16x32_bf16 v[140:143], v[168:171], v[200:203], v[140:143]
	v_mfma_f32_16x16x32_bf16 v[136:139], v[180:183], v[200:203], v[136:139]
	v_mfma_f32_16x16x32_bf16 v[132:135], v[184:187], v[200:203], v[132:135]
	v_cvt_pk_bf16_f32 v188, v7, v11
	buffer_load_dwordx4 v[4:7], v225, s[24:27], s7 offen
	buffer_load_dwordx4 v[8:11], v225, s[24:27], s8 offen
	s_add_i32 s7, s4, 0xffff6000
	v_cvt_pk_bf16_f32 v189, v15, v19
	s_add_i32 s8, s4, 0xffff8000
	buffer_load_dwordx4 v[12:15], v225, s[24:27], s7 offen
	buffer_load_dwordx4 v[16:19], v225, s[24:27], s8 offen
	s_add_i32 s7, s4, 0xffffa000
	v_cvt_pk_bf16_f32 v190, v23, v31
	s_add_i32 s8, s4, 0xffffc000
	buffer_load_dwordx4 v[20:23], v225, s[24:27], s7 offen
	buffer_load_dwordx4 v[28:31], v225, s[24:27], s8 offen
	s_add_i32 s7, s4, 0xffffe000
	v_cvt_pk_bf16_f32 v191, v27, v35
	buffer_load_dwordx4 v[24:27], v225, s[24:27], s7 offen
	buffer_load_dwordx4 v[32:35], v225, s[24:27], s4 offen
	s_waitcnt lgkmcnt(1)
	v_mfma_f32_16x16x32_bf16 v[128:131], v[164:167], v[204:207], v[128:131]
	v_mfma_f32_16x16x32_bf16 v[124:127], v[168:171], v[204:207], v[124:127]
	v_mfma_f32_16x16x32_bf16 v[120:123], v[180:183], v[204:207], v[120:123]
	v_mfma_f32_16x16x32_bf16 v[116:119], v[184:187], v[204:207], v[116:119]
	v_add_u32_e32 v192, v3, v220
	v_add_u32_e32 v3, v3, v218
	ds_write_b128 v192, v[172:175] offset:32768
	ds_write_b128 v192, v[228:231] offset:32832
	s_waitcnt lgkmcnt(2)
	v_mfma_f32_16x16x32_bf16 v[112:115], v[164:167], v[208:211], v[112:115]
	ds_write_b128 v192, v[232:235] offset:32896
	ds_write_b128 v3, v[188:191] offset:32768
	v_mfma_f32_16x16x32_bf16 v[108:111], v[168:171], v[208:211], v[108:111]
	v_mfma_f32_16x16x32_bf16 v[104:107], v[180:183], v[208:211], v[104:107]
	v_mfma_f32_16x16x32_bf16 v[100:103], v[184:187], v[208:211], v[100:103]
	s_waitcnt lgkmcnt(0)
	s_barrier
	s_add_i32 s4, s4, 0x80000
	s_addk_i32 s5, 0x80
	s_add_i32 s3, s3, 0x10000
	s_cmp_lg_u32 s4, 0x100e000
	s_cbranch_scc1 .LBB0_1265
	v_add_u32_e32 v3, 0, v226
	v_add_u32_e32 v204, 0, v216
	ds_read_b128 v[164:167], v3 offset:32768
	ds_read_b128 v[168:171], v3 offset:34816
	ds_read_b128 v[172:175], v3 offset:36864
	ds_read_b128 v[176:179], v3 offset:38912
	ds_read_b128 v[180:183], v204
	ds_read_b128 v[184:187], v204 offset:2048
	ds_read_b128 v[188:191], v204 offset:4096
	ds_read_b128 v[192:195], v204 offset:6144
	s_add_i32 m0, s1, 0x10000
	s_add_i32 s3, s1, 0x16000
	s_add_i32 s4, s1, 0x14000
	s_add_i32 s1, s1, 0x12000
	s_mov_b32 s38, s26
	s_mov_b32 s39, s27
	s_waitcnt lgkmcnt(3)
	v_mfma_f32_16x16x32_bf16 v[160:163], v[164:167], v[180:183], v[160:163]
	v_mfma_f32_16x16x32_bf16 v[156:159], v[168:171], v[180:183], v[156:159]
	v_mfma_f32_16x16x32_bf16 v[152:155], v[172:175], v[180:183], v[152:155]
	v_mfma_f32_16x16x32_bf16 v[148:151], v[176:179], v[180:183], v[148:151]
	s_waitcnt lgkmcnt(2)
	v_mfma_f32_16x16x32_bf16 v[144:147], v[164:167], v[184:187], v[144:147]
	v_mfma_f32_16x16x32_bf16 v[140:143], v[168:171], v[184:187], v[140:143]
	v_mfma_f32_16x16x32_bf16 v[136:139], v[172:175], v[184:187], v[136:139]
	v_mfma_f32_16x16x32_bf16 v[132:135], v[176:179], v[184:187], v[132:135]
	ds_read_b128 v[180:183], v204 offset:8192
	ds_read_b128 v[184:187], v204 offset:10240
	ds_read_b128 v[196:199], v204 offset:12288
	ds_read_b128 v[200:203], v204 offset:14336
	buffer_load_dwordx4 v223, s[36:39], s83 offen lds
	s_mov_b32 m0, s1
	s_waitcnt lgkmcnt(4)
	v_mfma_f32_16x16x32_bf16 v[112:115], v[164:167], v[192:195], v[112:115]
	buffer_load_dwordx4 v222, s[36:39], s83 offen lds
	s_mov_b32 m0, s4
	s_nop 0
	buffer_load_dwordx4 v221, s[36:39], s83 offen lds
	s_mov_b32 m0, s3
	v_mfma_f32_16x16x32_bf16 v[108:111], v[168:171], v[192:195], v[108:111]
	buffer_load_dwordx4 v224, s[36:39], s83 offen lds
	v_mfma_f32_16x16x32_bf16 v[104:107], v[172:175], v[192:195], v[104:107]
	v_mfma_f32_16x16x32_bf16 v[100:103], v[176:179], v[192:195], v[100:103]
	v_mfma_f32_16x16x32_bf16 v[128:131], v[164:167], v[188:191], v[128:131]
	v_mfma_f32_16x16x32_bf16 v[124:127], v[168:171], v[188:191], v[124:127]
	v_mfma_f32_16x16x32_bf16 v[120:123], v[172:175], v[188:191], v[120:123]
	v_mfma_f32_16x16x32_bf16 v[116:119], v[176:179], v[188:191], v[116:119]
	s_waitcnt lgkmcnt(3)
	v_mfma_f32_16x16x32_bf16 v[96:99], v[164:167], v[180:183], v[96:99]
	v_mfma_f32_16x16x32_bf16 v[92:95], v[168:171], v[180:183], v[92:95]
	v_mfma_f32_16x16x32_bf16 v[88:91], v[172:175], v[180:183], v[88:91]
	v_mfma_f32_16x16x32_bf16 v[84:87], v[176:179], v[180:183], v[84:87]
	s_waitcnt lgkmcnt(2)
	v_mfma_f32_16x16x32_bf16 v[80:83], v[164:167], v[184:187], v[80:83]
	v_mfma_f32_16x16x32_bf16 v[76:79], v[168:171], v[184:187], v[76:79]
	v_mfma_f32_16x16x32_bf16 v[72:75], v[172:175], v[184:187], v[72:75]
	v_mfma_f32_16x16x32_bf16 v[68:71], v[176:179], v[184:187], v[68:71]
	s_waitcnt lgkmcnt(1)
; #define G_DMA_A(buf, t, i_) __builtin_amdgcn_raw_ptr_buffer_load_lds(ra, (LAS void*)(lds + (buf) * 65536 + a_wu + (i_) * 8192), 16, ao##i_, (unsigned)(t) * 128u, 0, 0)
; #define G_ISSUE_B(t) do { const unsigned so_ = (unsigned)(t) * 64u * ldbB; _Pragma("unroll") for (int i_ = 0; i_ < 8; ++i_) sb[i_] = __builtin_bit_cast(f32x4, __builtin_amdgcn_raw_buffer_load_b128(rb, bo, so_ + (unsigned)i_ * ldbB, 0)); } while (0)
; #define G_RETIRE() asm volatile("s_waitcnt vmcnt(0)" : "+v"(sb[0]), "+v"(sb[1]), "+v"(sb[2]), "+v"(sb[3]), "+v"(sb[4]), "+v"(sb[5]), "+v"(sb[6]), "+v"(sb[7]) :: "memory")
; #define G_WRITE_B(buf) do { LAS unsigned char* d_ = lds + (buf) * 65536; \
;         _Pragma("unroll") for (int j_ = 0; j_ < 4; ++j_) { u32x4 w_; w_.x = cvtpk(sb[0][j_], sb[1][j_]); w_.y = cvtpk(sb[2][j_], sb[3][j_]); w_.z = cvtpk(sb[4][j_], sb[5][j_]); w_.w = cvtpk(sb[6][j_], sb[7][j_]); \
;             *(LAS u32x4*)(d_ + 32768 + T.b_w + ((T.b_rot + 64u * j_) & 255u)) = w_; } } while (0)
; #define G_LDB(dst, buf, ks) do { const LAS unsigned char* s_ = lds + (buf) * 65536 + (ks) * 1024; _Pragma("unroll") for (int n_ = 0; n_ < 4; ++n_) dst[n_] = *(const LAS bf16x8*)(s_ + T.b_r + n_ * 2048); } while (0)
; #define G_LDA(dst, buf, ks, h_) do { const LAS unsigned char* s_ = lds + (buf) * 65536 + (ks) * 1024; _Pragma("unroll") for (int m_ = 0; m_ < 4; ++m_) dst[m_] = *(const LAS bf16x8*)(s_ + T.a_r + ((h_) * 4 + m_) * 2048); } while (0)
; #define G_SB() __builtin_amdgcn_sched_barrier(0)
; #define G_BAR() do { asm volatile("s_waitcnt lgkmcnt(0)" ::: "memory"); __builtin_amdgcn_s_barrier(); asm volatile("" ::: "memory"); } while (0)
; __device__ __forceinline__ void gemm_kloop(f32x4 (&acc)[8][4], LAS unsigned char* lds, const GemmT& T, ...
;     ...
;     for (int t = 0; t < nt; ++t) { const int cur = t & 1; const bool w1 = t + 1 < nt, i2 = t + 2 < nt;
;         G_LDB(Bf0, cur, 0); G_LDA(AtA, cur, 0, 0); G_SB();
;         G_LDA(AtB, cur, 0, 1); if (w1) { G_DMA_A(cur ^ 1, t + 1, 0); G_DMA_A(cur ^ 1, t + 1, 1); G_DMA_A(cur ^ 1, t + 1, 2); G_DMA_A(cur ^ 1, t + 1, 3); } G_MMA(AtA, Bf0, 0); G_SB();
;         G_LDB(Bf1, cur, 1); G_LDA(AtA, cur, 1, 0); G_MMA(AtB, Bf0, 1); G_SB();
;         G_LDA(AtB, cur, 1, 1); if (w1) { G_RETIRE(); G_WRITE_B(cur ^ 1); } if (i2) G_ISSUE_B(t + 2); G_MMA(AtA, Bf1, 0); G_SB();
;         G_MMA(AtB, Bf1, 1); G_SB();
;         G_BAR(); }
	v_mfma_f32_16x16x32_bf16 v[64:67], v[164:167], v[196:199], v[64:67]
	v_mfma_f32_16x16x32_bf16 v[60:63], v[168:171], v[196:199], v[60:63]
	v_mfma_f32_16x16x32_bf16 v[56:59], v[172:175], v[196:199], v[56:59]
	v_mfma_f32_16x16x32_bf16 v[52:55], v[176:179], v[196:199], v[52:55]
	s_waitcnt lgkmcnt(0)
	v_mfma_f32_16x16x32_bf16 v[48:51], v[164:167], v[200:203], v[48:51]
	v_mfma_f32_16x16x32_bf16 v[44:47], v[168:171], v[200:203], v[44:47]
	ds_read_b128 v[164:167], v3 offset:33792
	ds_read_b128 v[168:171], v3 offset:35840
	ds_read_b128 v[180:183], v3 offset:37888
	ds_read_b128 v[184:187], v3 offset:39936
	v_mfma_f32_16x16x32_bf16 v[40:43], v[172:175], v[200:203], v[40:43]
	ds_read_b128 v[172:175], v204 offset:1024
	ds_read_b128 v[188:191], v204 offset:3072
	ds_read_b128 v[192:195], v204 offset:5120
	ds_read_b128 v[196:199], v204 offset:7168
	v_mfma_f32_16x16x32_bf16 v[36:39], v[176:179], v[200:203], v[36:39]
	s_waitcnt lgkmcnt(3)
	v_mfma_f32_16x16x32_bf16 v[160:163], v[164:167], v[172:175], v[160:163]
	v_add_u32_e32 v3, s29, v219
	v_mfma_f32_16x16x32_bf16 v[156:159], v[168:171], v[172:175], v[156:159]
	v_mfma_f32_16x16x32_bf16 v[152:155], v[180:183], v[172:175], v[152:155]
	v_mfma_f32_16x16x32_bf16 v[148:151], v[184:187], v[172:175], v[148:151]
	ds_read_b128 v[172:175], v204 offset:9216
	ds_read_b128 v[176:179], v204 offset:11264
	ds_read_b128 v[200:203], v204 offset:13312
	ds_read_b128 v[204:207], v204 offset:15360
	s_waitcnt vmcnt(4)
	s_waitcnt vmcnt(0)
	s_waitcnt lgkmcnt(6)
	v_mfma_f32_16x16x32_bf16 v[144:147], v[164:167], v[188:191], v[144:147]
	v_mfma_f32_16x16x32_bf16 v[140:143], v[168:171], v[188:191], v[140:143]
	v_mfma_f32_16x16x32_bf16 v[136:139], v[180:183], v[188:191], v[136:139]
	v_mfma_f32_16x16x32_bf16 v[132:135], v[184:187], v[188:191], v[132:135]
	v_cvt_pk_bf16_f32 v188, v4, v8
	v_cvt_pk_bf16_f32 v189, v12, v16
	v_cvt_pk_bf16_f32 v190, v20, v28
	v_cvt_pk_bf16_f32 v191, v24, v32
	v_add_u32_e32 v4, v3, v220
	ds_write_b128 v4, v[188:191]
	v_cvt_pk_bf16_f32 v188, v5, v9
	v_cvt_pk_bf16_f32 v189, v13, v17
	v_cvt_pk_bf16_f32 v190, v21, v29
	v_cvt_pk_bf16_f32 v191, v25, v33
	ds_write_b128 v4, v[188:191] offset:64
	v_cvt_pk_bf16_f32 v188, v6, v10
	v_cvt_pk_bf16_f32 v189, v14, v18
	v_cvt_pk_bf16_f32 v190, v22, v30
	v_cvt_pk_bf16_f32 v191, v26, v34
	ds_write_b128 v4, v[188:191] offset:128
	v_cvt_pk_bf16_f32 v4, v7, v11
	v_cvt_pk_bf16_f32 v5, v15, v19
	v_cvt_pk_bf16_f32 v6, v23, v31
	v_cvt_pk_bf16_f32 v7, v27, v35
	v_add_u32_e32 v3, v3, v218
	s_waitcnt lgkmcnt(7)
	v_mfma_f32_16x16x32_bf16 v[112:115], v[164:167], v[196:199], v[112:115]
	ds_write_b128 v3, v[4:7]
	v_mfma_f32_16x16x32_bf16 v[108:111], v[168:171], v[196:199], v[108:111]
	v_mfma_f32_16x16x32_bf16 v[8:11], v[180:183], v[196:199], v[104:107]
	v_mfma_f32_16x16x32_bf16 v[4:7], v[184:187], v[196:199], v[100:103]
	v_mfma_f32_16x16x32_bf16 v[128:131], v[164:167], v[192:195], v[128:131]
	v_mfma_f32_16x16x32_bf16 v[124:127], v[168:171], v[192:195], v[124:127]
	v_mfma_f32_16x16x32_bf16 v[120:123], v[180:183], v[192:195], v[120:123]
	v_mfma_f32_16x16x32_bf16 v[116:119], v[184:187], v[192:195], v[116:119]
	s_waitcnt lgkmcnt(7)
	v_mfma_f32_16x16x32_bf16 v[12:15], v[164:167], v[172:175], v[96:99]
	v_mfma_f32_16x16x32_bf16 v[16:19], v[168:171], v[172:175], v[92:95]
	v_mfma_f32_16x16x32_bf16 v[20:23], v[180:183], v[172:175], v[88:91]
	v_mfma_f32_16x16x32_bf16 v[24:27], v[184:187], v[172:175], v[84:87]
	s_waitcnt lgkmcnt(6)
	v_mfma_f32_16x16x32_bf16 v[28:31], v[164:167], v[176:179], v[80:83]
	v_mfma_f32_16x16x32_bf16 v[32:35], v[168:171], v[176:179], v[76:79]
	v_mfma_f32_16x16x32_bf16 v[72:75], v[180:183], v[176:179], v[72:75]
	v_mfma_f32_16x16x32_bf16 v[68:71], v[184:187], v[176:179], v[68:71]
	s_waitcnt lgkmcnt(5)
	v_mfma_f32_16x16x32_bf16 v[64:67], v[164:167], v[200:203], v[64:67]
	v_mfma_f32_16x16x32_bf16 v[60:63], v[168:171], v[200:203], v[60:63]
	v_mfma_f32_16x16x32_bf16 v[56:59], v[180:183], v[200:203], v[56:59]
	v_mfma_f32_16x16x32_bf16 v[52:55], v[184:187], v[200:203], v[52:55]
	s_waitcnt lgkmcnt(4)
	v_mfma_f32_16x16x32_bf16 v[48:51], v[164:167], v[204:207], v[48:51]
	v_mfma_f32_16x16x32_bf16 v[44:47], v[168:171], v[204:207], v[44:47]
	v_mfma_f32_16x16x32_bf16 v[40:43], v[180:183], v[204:207], v[40:43]
	v_mfma_f32_16x16x32_bf16 v[36:39], v[184:187], v[204:207], v[36:39]
	s_add_i32 s1, 0, 0x10000
	s_waitcnt lgkmcnt(0)
	s_barrier
; #define G_DMA_A(buf, t, i_) __builtin_amdgcn_raw_ptr_buffer_load_lds(ra, (LAS void*)(lds + (buf) * 65536 + a_wu + (i_) * 8192), 16, ao##i_, (unsigned)(t) * 128u, 0, 0)
; #define G_ISSUE_B(t) do { const unsigned so_ = (unsigned)(t) * 64u * ldbB; _Pragma("unroll") for (int i_ = 0; i_ < 8; ++i_) sb[i_] = __builtin_bit_cast(f32x4, __builtin_amdgcn_raw_buffer_load_b128(rb, bo, so_ + (unsigned)i_ * ldbB, 0)); } while (0)
; #define G_RETIRE() asm volatile("s_waitcnt vmcnt(0)" : "+v"(sb[0]), "+v"(sb[1]), "+v"(sb[2]), "+v"(sb[3]), "+v"(sb[4]), "+v"(sb[5]), "+v"(sb[6]), "+v"(sb[7]) :: "memory")
; #define G_WRITE_B(buf) do { LAS unsigned char* d_ = lds + (buf) * 65536; \
;         _Pragma("unroll") for (int j_ = 0; j_ < 4; ++j_) { u32x4 w_; w_.x = cvtpk(sb[0][j_], sb[1][j_]); w_.y = cvtpk(sb[2][j_], sb[3][j_]); w_.z = cvtpk(sb[4][j_], sb[5][j_]); w_.w = cvtpk(sb[6][j_], sb[7][j_]); \
;             *(LAS u32x4*)(d_ + 32768 + T.b_w + ((T.b_rot + 64u * j_) & 255u)) = w_; } } while (0)
; #define G_LDB(dst, buf, ks) do { const LAS unsigned char* s_ = lds + (buf) * 65536 + (ks) * 1024; _Pragma("unroll") for (int n_ = 0; n_ < 4; ++n_) dst[n_] = *(const LAS bf16x8*)(s_ + T.b_r + n_ * 2048); } while (0)
; #define G_LDA(dst, buf, ks, h_) do { const LAS unsigned char* s_ = lds + (buf) * 65536 + (ks) * 1024; _Pragma("unroll") for (int m_ = 0; m_ < 4; ++m_) dst[m_] = *(const LAS bf16x8*)(s_ + T.a_r + ((h_) * 4 + m_) * 2048); } while (0)
; #define G_SB() __builtin_amdgcn_sched_barrier(0)
; #define G_BAR() do { asm volatile("s_waitcnt lgkmcnt(0)" ::: "memory"); __builtin_amdgcn_s_barrier(); asm volatile("" ::: "memory"); } while (0)
; __device__ __forceinline__ void gemm_kloop(f32x4 (&acc)[8][4], LAS unsigned char* lds, const GemmT& T, ...
;     ...
;     for (int t = 0; t < nt; ++t) { const int cur = t & 1; const bool w1 = t + 1 < nt, i2 = t + 2 < nt;
;         G_LDB(Bf0, cur, 0); G_LDA(AtA, cur, 0, 0); G_SB();
;         G_LDA(AtB, cur, 0, 1); if (w1) { G_DMA_A(cur ^ 1, t + 1, 0); G_DMA_A(cur ^ 1, t + 1, 1); G_DMA_A(cur ^ 1, t + 1, 2); G_DMA_A(cur ^ 1, t + 1, 3); } G_MMA(AtA, Bf0, 0); G_SB();
;         G_LDB(Bf1, cur, 1); G_LDA(AtA, cur, 1, 0); G_MMA(AtB, Bf0, 1); G_SB();
;         G_LDA(AtB, cur, 1, 1); if (w1) { G_RETIRE(); G_WRITE_B(cur ^ 1); } if (i2) G_ISSUE_B(t + 2); G_MMA(AtA, Bf1, 0); G_SB();
;         G_MMA(AtB, Bf1, 1); G_SB();
;         G_BAR(); }
	v_add_u32_e32 v3, s1, v217
	ds_read_b128 v[76:79], v3
	ds_read_b128 v[80:83], v3 offset:2048
	ds_read_b128 v[84:87], v3 offset:4096
	ds_read_b128 v[88:91], v3 offset:6144
	v_add_u32_e32 v3, s1, v216
	ds_read_b128 v[92:95], v3
	ds_read_b128 v[96:99], v3 offset:2048
	ds_read_b128 v[100:103], v3 offset:4096
	ds_read_b128 v[104:107], v3 offset:6144
	s_waitcnt lgkmcnt(2)
	v_mfma_f32_16x16x32_bf16 v[144:147], v[76:79], v[96:99], v[144:147]
	v_mfma_f32_16x16x32_bf16 v[140:143], v[80:83], v[96:99], v[140:143]
	v_mfma_f32_16x16x32_bf16 v[172:175], v[84:87], v[96:99], v[136:139]
	v_mfma_f32_16x16x32_bf16 v[96:99], v[88:91], v[96:99], v[132:135]
	s_waitcnt lgkmcnt(1)
	v_mfma_f32_16x16x32_bf16 v[128:131], v[76:79], v[100:103], v[128:131]
	v_mfma_f32_16x16x32_bf16 v[124:127], v[80:83], v[100:103], v[124:127]
	v_mfma_f32_16x16x32_bf16 v[120:123], v[84:87], v[100:103], v[120:123]
	v_mfma_f32_16x16x32_bf16 v[116:119], v[88:91], v[100:103], v[116:119]
	s_waitcnt lgkmcnt(0)
	v_mfma_f32_16x16x32_bf16 v[132:135], v[76:79], v[104:107], v[112:115]
	v_mfma_f32_16x16x32_bf16 v[176:179], v[80:83], v[104:107], v[108:111]
	ds_read_b128 v[100:103], v3 offset:8192
	s_nop 1
	ds_read_b128 v[108:111], v3 offset:10240
	ds_read_b128 v[112:115], v3 offset:12288
	ds_read_b128 v[136:139], v3 offset:14336
	v_mfma_f32_16x16x32_bf16 v[160:163], v[76:79], v[92:95], v[160:163]
	v_mfma_f32_16x16x32_bf16 v[164:167], v[80:83], v[92:95], v[156:159]
	v_mfma_f32_16x16x32_bf16 v[168:171], v[84:87], v[92:95], v[152:155]
	v_mfma_f32_16x16x32_bf16 v[92:95], v[88:91], v[92:95], v[148:151]
	v_mfma_f32_16x16x32_bf16 v[8:11], v[84:87], v[104:107], v[8:11]
	v_mfma_f32_16x16x32_bf16 v[4:7], v[88:91], v[104:107], v[4:7]
	v_add_u32_e32 v3, s64, v217
	ds_read_b128 v[218:221], v3
	ds_read_b128 v[222:225], v3 offset:2048
	ds_read_b128 v[230:233], v3 offset:4096
	ds_read_b128 v[234:237], v3 offset:6144
	v_add_u32_e32 v3, s64, v216
	s_waitcnt lgkmcnt(5)
	v_mfma_f32_16x16x32_bf16 v[206:209], v[88:91], v[112:115], v[52:55]
	s_waitcnt lgkmcnt(4)
	v_mfma_f32_16x16x32_bf16 v[210:213], v[76:79], v[136:139], v[48:51]
	v_mfma_f32_16x16x32_bf16 v[226:229], v[80:83], v[136:139], v[44:47]
	v_mfma_f32_16x16x32_bf16 v[238:241], v[84:87], v[136:139], v[40:43]
	s_nop 2
	ds_read_b128 v[40:43], v3
	ds_read_b128 v[44:47], v3 offset:2048
	ds_read_b128 v[48:51], v3 offset:4096
	ds_read_b128 v[52:55], v3 offset:6144
	v_mfma_f32_16x16x32_bf16 v[12:15], v[76:79], v[100:103], v[12:15]
	v_mfma_f32_16x16x32_bf16 v[16:19], v[80:83], v[100:103], v[16:19]
	v_mfma_f32_16x16x32_bf16 v[20:23], v[84:87], v[100:103], v[20:23]
	v_mfma_f32_16x16x32_bf16 v[24:27], v[88:91], v[100:103], v[24:27]
	v_mfma_f32_16x16x32_bf16 v[28:31], v[76:79], v[108:111], v[28:31]
	v_mfma_f32_16x16x32_bf16 v[32:35], v[80:83], v[108:111], v[32:35]
	v_mfma_f32_16x16x32_bf16 v[180:183], v[84:87], v[108:111], v[72:75]
	v_mfma_f32_16x16x32_bf16 v[184:187], v[88:91], v[108:111], v[68:71]
	v_mfma_f32_16x16x32_bf16 v[188:191], v[76:79], v[112:115], v[64:67]
	v_mfma_f32_16x16x32_bf16 v[198:201], v[80:83], v[112:115], v[60:63]
	v_mfma_f32_16x16x32_bf16 v[202:205], v[84:87], v[112:115], v[56:59]
	v_mfma_f32_16x16x32_bf16 v[242:245], v[88:91], v[136:139], v[36:39]
	s_waitcnt lgkmcnt(3)
	v_mfma_f32_16x16x32_bf16 v[154:157], v[218:221], v[40:43], v[160:163]
	v_mfma_f32_16x16x32_bf16 v[158:161], v[234:237], v[40:43], v[92:95]
	s_waitcnt lgkmcnt(2)
	v_mfma_f32_16x16x32_bf16 v[106:109], v[218:221], v[44:47], v[144:147]
	v_mfma_f32_16x16x32_bf16 v[138:141], v[222:225], v[44:47], v[140:143]
	v_mfma_f32_16x16x32_bf16 v[102:105], v[230:233], v[44:47], v[172:175]
	v_mfma_f32_16x16x32_bf16 v[110:113], v[234:237], v[44:47], v[96:99]
	s_waitcnt lgkmcnt(1)
	v_mfma_f32_16x16x32_bf16 v[90:93], v[218:221], v[48:51], v[128:131]
	v_mfma_f32_16x16x32_bf16 v[98:101], v[222:225], v[48:51], v[124:127]
	v_mfma_f32_16x16x32_bf16 v[86:89], v[230:233], v[48:51], v[120:123]
	v_mfma_f32_16x16x32_bf16 v[94:97], v[234:237], v[48:51], v[116:119]
	s_waitcnt lgkmcnt(0)
	v_mfma_f32_16x16x32_bf16 v[70:73], v[230:233], v[52:55], v[8:11]
	s_nop 2
	ds_read_b128 v[8:11], v3 offset:8192
	ds_read_b128 v[46:49], v3 offset:10240
	ds_read_b128 v[114:117], v3 offset:12288
	ds_read_b128 v[118:121], v3 offset:14336
	v_mfma_f32_16x16x32_bf16 v[194:197], v[222:225], v[40:43], v[164:167]
	v_mfma_f32_16x16x32_bf16 v[150:153], v[230:233], v[40:43], v[168:171]
	v_mfma_f32_16x16x32_bf16 v[74:77], v[218:221], v[52:55], v[132:135]
	v_mfma_f32_16x16x32_bf16 v[82:85], v[222:225], v[52:55], v[176:179]
	v_mfma_f32_16x16x32_bf16 v[78:81], v[234:237], v[52:55], v[4:7]
	s_waitcnt lgkmcnt(3)
	v_mfma_f32_16x16x32_bf16 v[58:61], v[218:221], v[8:11], v[12:15]
	v_mfma_f32_16x16x32_bf16 v[66:69], v[222:225], v[8:11], v[16:19]
	v_mfma_f32_16x16x32_bf16 v[54:57], v[230:233], v[8:11], v[20:23]
	v_mfma_f32_16x16x32_bf16 v[62:65], v[234:237], v[8:11], v[24:27]
	s_waitcnt lgkmcnt(2)
	v_mfma_f32_16x16x32_bf16 v[42:45], v[218:221], v[46:49], v[28:31]
	v_mfma_f32_16x16x32_bf16 v[50:53], v[222:225], v[46:49], v[32:35]
	v_mfma_f32_16x16x32_bf16 v[38:41], v[230:233], v[46:49], v[180:183]
	v_mfma_f32_16x16x32_bf16 v[46:49], v[234:237], v[46:49], v[184:187]
	s_waitcnt lgkmcnt(1)
	v_mfma_f32_16x16x32_bf16 v[26:29], v[218:221], v[114:117], v[188:191]
	v_mfma_f32_16x16x32_bf16 v[34:37], v[222:225], v[114:117], v[198:201]
	v_mfma_f32_16x16x32_bf16 v[22:25], v[230:233], v[114:117], v[202:205]
	v_mfma_f32_16x16x32_bf16 v[30:33], v[234:237], v[114:117], v[206:209]
	s_waitcnt lgkmcnt(0)
	v_mfma_f32_16x16x32_bf16 v[10:13], v[218:221], v[118:121], v[210:213]
	v_mfma_f32_16x16x32_bf16 v[18:21], v[222:225], v[118:121], v[226:229]
	v_mfma_f32_16x16x32_bf16 v[6:9], v[230:233], v[118:121], v[238:241]
	v_mfma_f32_16x16x32_bf16 v[14:17], v[234:237], v[118:121], v[242:245]
	s_waitcnt lgkmcnt(0)
	s_barrier

; #define G_DMA_A(buf, t, i_) __builtin_amdgcn_raw_ptr_buffer_load_lds(ra, (LAS void*)(lds + (buf) * 65536 + a_wu + (i_) * 8192), 16, ao##i_, (unsigned)(t) * 128u, 0, 0)
; #define G_ISSUE_B(t) do { const unsigned so_ = (unsigned)(t) * 64u * ldbB; _Pragma("unroll") for (int i_ = 0; i_ < 8; ++i_) sb[i_] = __builtin_bit_cast(f32x4, __builtin_amdgcn_raw_buffer_load_b128(rb, bo, so_ + (unsigned)i_ * ldbB, 0)); } while (0)
; #define G_RETIRE() asm volatile("s_waitcnt vmcnt(0)" : "+v"(sb[0]), "+v"(sb[1]), "+v"(sb[2]), "+v"(sb[3]), "+v"(sb[4]), "+v"(sb[5]), "+v"(sb[6]), "+v"(sb[7]) :: "memory")
; #define G_WRITE_B(buf) do { LAS unsigned char* d_ = lds + (buf) * 65536; \
;         _Pragma("unroll") for (int j_ = 0; j_ < 4; ++j_) { u32x4 w_; w_.x = cvtpk(sb[0][j_], sb[1][j_]); w_.y = cvtpk(sb[2][j_], sb[3][j_]); w_.z = cvtpk(sb[4][j_], sb[5][j_]); w_.w = cvtpk(sb[6][j_], sb[7][j_]); \
;             *(LAS u32x4*)(d_ + 32768 + T.b_w + ((T.b_rot + 64u * j_) & 255u)) = w_; } } while (0)
; #define G_BAR() do { asm volatile("s_waitcnt lgkmcnt(0)" ::: "memory"); __builtin_amdgcn_s_barrier(); asm volatile("" ::: "memory"); } while (0)
; #define G_DMA_A(buf, t, i_) __builtin_amdgcn_raw_ptr_buffer_load_lds(ra, (LAS void*)(lds + (buf) * 65536 + a_wu + (i_) * 8192), 16, ao##i_, (unsigned)(t) * 128u, 0, 0)
; #define G_ISSUE_B(t) do { const unsigned so_ = (unsigned)(t) * 64u * ldbB; _Pragma("unroll") for (int i_ = 0; i_ < 8; ++i_) sb[i_] = __builtin_bit_cast(f32x4, __builtin_amdgcn_raw_buffer_load_b128(rb, bo, so_ + (unsigned)i_ * ldbB, 0)); } while (0)
; #define G_RETIRE() asm volatile("s_waitcnt vmcnt(0)" : "+v"(sb[0]), "+v"(sb[1]), "+v"(sb[2]), "+v"(sb[3]), "+v"(sb[4]), "+v"(sb[5]), "+v"(sb[6]), "+v"(sb[7]) :: "memory")
; __device__ __forceinline__ void gemm_kloop(f32x4 (&acc)[8][4], LAS unsigned char* lds, const GemmT& T, ...
;     ...
;     G_ISSUE_B(0); G_DMA_A(0, 0, 0); G_DMA_A(0, 0, 1); G_DMA_A(0, 0, 2); G_DMA_A(0, 0, 3); G_RETIRE(); G_WRITE_B(0);
;     if (nt > 1) G_ISSUE_B(1);
;     G_BAR();
; __device__ __forceinline__ void acc_zero(f32x4 (&acc)[8][4]) {
; #pragma unroll
;     for (int m = 0; m < 8; ++m)
; #pragma unroll
;         for (int n = 0; n < 4; ++n) acc[m][n] = (f32x4){0.f, 0.f, 0.f, 0.f};
.LBB0_1574:
	s_cbranch_execz .LBB0_1578
	s_sub_i32 s98, s83, s85
	s_sub_i32 s98, s98, 0x81
	s_lshr_b32 s98, s98, 5
	s_sub_i32 s98, s98, 1
	s_max_i32 s98, s98, 0
	s_min_i32 s98, s98, 2
	s_cmp_eq_u32 s1, 0
	s_cselect_b32 s98, 2, s98
	v_readfirstlane_b32 s1, v230
	s_and_b32 s1, s1, 0xfffffc00
	s_add_i32 s1, s1, 0
	s_mov_b32 s38, s26
	s_mov_b32 s39, s27
	s_mov_b32 m0, s1
	v_add_u32_e32 v3, v228, v221
	buffer_load_dwordx4 v225, s[36:39], 0 offen lds
	s_add_i32 m0, s1, 0x2000
	v_mov_b32_e32 v36, 0
	buffer_load_dwordx4 v226, s[36:39], 0 offen lds
	s_add_i32 m0, s1, 0x4000
	s_mov_b32 s2, 0
	buffer_load_dwordx4 v224, s[36:39], 0 offen lds
	s_add_i32 m0, s1, 0x6000
	s_mov_b32 s3, 0x10e000
	buffer_load_dwordx4 v223, s[36:39], 0 offen lds
	s_waitcnt vmcnt(4)
	s_waitcnt vmcnt(0)
	s_movk_i32 s4, 0x80
	v_cvt_pk_bf16_f32 v4, v110, v122
	v_cvt_pk_bf16_f32 v5, v126, v114
	v_cvt_pk_bf16_f32 v6, v118, v130
	v_cvt_pk_bf16_f32 v7, v138, v142
	ds_write_b128 v229, v[4:7] offset:32768
	v_cvt_pk_bf16_f32 v4, v111, v123
	v_cvt_pk_bf16_f32 v5, v127, v115
	v_cvt_pk_bf16_f32 v6, v119, v131
	v_cvt_pk_bf16_f32 v7, v139, v143
	ds_write_b128 v229, v[4:7] offset:32832
	v_cvt_pk_bf16_f32 v4, v112, v124
	v_cvt_pk_bf16_f32 v5, v128, v116
	v_cvt_pk_bf16_f32 v6, v120, v132
	v_cvt_pk_bf16_f32 v7, v140, v144
	ds_write_b128 v229, v[4:7] offset:32896
	v_cvt_pk_bf16_f32 v4, v113, v125
	v_cvt_pk_bf16_f32 v5, v129, v117
	v_cvt_pk_bf16_f32 v6, v121, v133
	v_cvt_pk_bf16_f32 v7, v141, v145
	ds_write_b128 v3, v[4:7] offset:32768
	buffer_load_dwordx4 v[4:7], v222, s[24:27], s67 offen
	buffer_load_dwordx4 v[8:11], v222, s[24:27], s68 offen
	buffer_load_dwordx4 v[12:15], v222, s[24:27], s69 offen
	buffer_load_dwordx4 v[16:19], v222, s[24:27], s70 offen
	buffer_load_dwordx4 v[20:23], v222, s[24:27], s71 offen
	buffer_load_dwordx4 v[28:31], v222, s[24:27], s76 offen
	buffer_load_dwordx4 v[24:27], v222, s[24:27], s77 offen
	buffer_load_dwordx4 v[32:35], v222, s[24:27], s78 offen
	s_waitcnt lgkmcnt(0)
	s_barrier
	v_mov_b32_e32 v37, v36
	v_mov_b32_e32 v38, v36
	v_mov_b32_e32 v39, v36
	v_mov_b32_e32 v40, v36
	v_mov_b32_e32 v41, v36
	v_mov_b32_e32 v42, v36
	v_mov_b32_e32 v43, v36
	v_mov_b32_e32 v44, v36
	v_mov_b32_e32 v45, v36
	v_mov_b32_e32 v46, v36
	v_mov_b32_e32 v47, v36
	v_mov_b32_e32 v48, v36
	v_mov_b32_e32 v49, v36
	v_mov_b32_e32 v50, v36
	v_mov_b32_e32 v51, v36
	v_mov_b32_e32 v52, v36
	v_mov_b32_e32 v53, v36
	v_mov_b32_e32 v54, v36
	v_mov_b32_e32 v55, v36
	v_mov_b32_e32 v56, v36
	v_mov_b32_e32 v57, v36
	v_mov_b32_e32 v58, v36
	v_mov_b32_e32 v59, v36
	v_mov_b32_e32 v60, v36
	v_mov_b32_e32 v61, v36
	v_mov_b32_e32 v62, v36
	v_mov_b32_e32 v63, v36
	v_mov_b32_e32 v64, v36
	v_mov_b32_e32 v65, v36
	v_mov_b32_e32 v66, v36
	v_mov_b32_e32 v67, v36
	v_mov_b32_e32 v68, v36
	v_mov_b32_e32 v69, v36
	v_mov_b32_e32 v70, v36
	v_mov_b32_e32 v71, v36
	v_mov_b32_e32 v72, v36
	v_mov_b32_e32 v73, v36
	v_mov_b32_e32 v74, v36
	v_mov_b32_e32 v75, v36
	v_mov_b32_e32 v76, v36
	v_mov_b32_e32 v77, v36
	v_mov_b32_e32 v78, v36
	v_mov_b32_e32 v79, v36
	v_mov_b32_e32 v80, v36
	v_mov_b32_e32 v81, v36
	v_mov_b32_e32 v82, v36
	v_mov_b32_e32 v83, v36
	v_mov_b32_e32 v84, v36
	v_mov_b32_e32 v85, v36
	v_mov_b32_e32 v86, v36
	v_mov_b32_e32 v87, v36
	v_mov_b32_e32 v88, v36
	v_mov_b32_e32 v89, v36
	v_mov_b32_e32 v90, v36
	v_mov_b32_e32 v91, v36
	v_mov_b32_e32 v92, v36
	v_mov_b32_e32 v93, v36
	v_mov_b32_e32 v94, v36
	v_mov_b32_e32 v95, v36
	v_mov_b32_e32 v96, v36
	v_mov_b32_e32 v97, v36
	v_mov_b32_e32 v98, v36
	v_mov_b32_e32 v99, v36
	v_mov_b32_e32 v100, v36
	v_mov_b32_e32 v101, v36
	v_mov_b32_e32 v102, v36
	v_mov_b32_e32 v103, v36
	v_mov_b32_e32 v104, v36
	v_mov_b32_e32 v105, v36
	v_mov_b32_e32 v106, v36
	v_mov_b32_e32 v107, v36
	v_mov_b32_e32 v108, v36
	v_mov_b32_e32 v109, v36
	v_mov_b32_e32 v110, v36
	v_mov_b32_e32 v111, v36
	v_mov_b32_e32 v112, v36
	v_mov_b32_e32 v113, v36
	v_mov_b32_e32 v114, v36
	v_mov_b32_e32 v115, v36
	v_mov_b32_e32 v116, v36
	v_mov_b32_e32 v117, v36
	v_mov_b32_e32 v118, v36
	v_mov_b32_e32 v119, v36
	v_mov_b32_e32 v120, v36
	v_mov_b32_e32 v121, v36
	v_mov_b32_e32 v122, v36
	v_mov_b32_e32 v123, v36
	v_mov_b32_e32 v124, v36
	v_mov_b32_e32 v125, v36
	v_mov_b32_e32 v126, v36
	v_mov_b32_e32 v127, v36
	v_mov_b32_e32 v128, v36
	v_mov_b32_e32 v129, v36
	v_mov_b32_e32 v130, v36
	v_mov_b32_e32 v131, v36
	v_mov_b32_e32 v132, v36
	v_mov_b32_e32 v133, v36
	v_mov_b32_e32 v134, v36
	v_mov_b32_e32 v135, v36
	v_mov_b32_e32 v136, v36
	v_mov_b32_e32 v137, v36
	v_mov_b32_e32 v138, v36
	v_mov_b32_e32 v139, v36
	v_mov_b32_e32 v140, v36
	v_mov_b32_e32 v141, v36
	v_mov_b32_e32 v142, v36
	v_mov_b32_e32 v143, v36
	v_mov_b32_e32 v144, v36
	v_mov_b32_e32 v145, v36
	v_mov_b32_e32 v146, v36
	v_mov_b32_e32 v147, v36
	v_mov_b32_e32 v148, v36
	v_mov_b32_e32 v149, v36
	v_mov_b32_e32 v150, v36
	v_mov_b32_e32 v151, v36
	v_mov_b32_e32 v152, v36
	v_mov_b32_e32 v153, v36
	v_mov_b32_e32 v154, v36
	v_mov_b32_e32 v155, v36
	v_mov_b32_e32 v156, v36
	v_mov_b32_e32 v157, v36
	v_mov_b32_e32 v158, v36
	v_mov_b32_e32 v159, v36
	v_mov_b32_e32 v160, v36
	v_mov_b32_e32 v161, v36
	v_mov_b32_e32 v162, v36
	v_mov_b32_e32 v163, v36
; #define G_DMA_A(buf, t, i_) __builtin_amdgcn_raw_ptr_buffer_load_lds(ra, (LAS void*)(lds + (buf) * 65536 + a_wu + (i_) * 8192), 16, ao##i_, (unsigned)(t) * 128u, 0, 0)
; #define G_LDB(dst, buf, ks) do { const LAS unsigned char* s_ = lds + (buf) * 65536 + (ks) * 1024; _Pragma("unroll") for (int n_ = 0; n_ < 4; ++n_) dst[n_] = *(const LAS bf16x8*)(s_ + T.b_r + n_ * 2048); } while (0)
; #define G_LDA(dst, buf, ks, h_) do { const LAS unsigned char* s_ = lds + (buf) * 65536 + (ks) * 1024; _Pragma("unroll") for (int m_ = 0; m_ < 4; ++m_) dst[m_] = *(const LAS bf16x8*)(s_ + T.a_r + ((h_) * 4 + m_) * 2048); } while (0)
; #define G_MMA(At_, Bf_, h_) do { _Pragma("unroll") for (int m_ = 0; m_ < 4; ++m_) _Pragma("unroll") for (int n_ = 0; n_ < 4; ++n_) \
;         acc[(h_) * 4 + m_][n_] = __builtin_amdgcn_mfma_f32_16x16x32_bf16(Bf_[n_], At_[m_], acc[(h_) * 4 + m_][n_], 0, 0, 0); } while (0)
; #define G_SB() __builtin_amdgcn_sched_barrier(0)
; #define G_DMA_A(buf, t, i_) __builtin_amdgcn_raw_ptr_buffer_load_lds(ra, (LAS void*)(lds + (buf) * 65536 + a_wu + (i_) * 8192), 16, ao##i_, (unsigned)(t) * 128u, 0, 0)
; __device__ __forceinline__ void gemm_kloop(f32x4 (&acc)[8][4], LAS unsigned char* lds, const GemmT& T, ...
;     ...
;     for (int t = 0; t < nt; ++t) { const int cur = t & 1; const bool w1 = t + 1 < nt, i2 = t + 2 < nt;
;         G_LDB(Bf0, cur, 0); G_LDA(AtA, cur, 0, 0); G_SB();
;         G_LDA(AtB, cur, 0, 1); if (w1) { G_DMA_A(cur ^ 1, t + 1, 0); G_DMA_A(cur ^ 1, t + 1, 1); G_DMA_A(cur ^ 1, t + 1, 2); G_DMA_A(cur ^ 1, t + 1, 3); } G_MMA(AtA, Bf0, 0); G_SB();
;         G_LDB(Bf1, cur, 1); G_LDA(AtA, cur, 1, 0); G_MMA(AtB, Bf0, 1); G_SB();
.LBB0_1576:
	s_and_b32 s5, s2, 0x10000
	s_add_i32 s6, s5, 0
	v_add_u32_e32 v3, s6, v227
	v_add_u32_e32 v208, s6, v217
	ds_read_b128 v[164:167], v3 offset:32768
	ds_read_b128 v[168:171], v3 offset:34816
	ds_read_b128 v[172:175], v3 offset:36864
	ds_read_b128 v[176:179], v3 offset:38912
	ds_read_b128 v[180:183], v208
	ds_read_b128 v[184:187], v208 offset:2048
	ds_read_b128 v[188:191], v208 offset:4096
	ds_read_b128 v[192:195], v208 offset:6144
	s_xor_b32 s5, s5, 0x10000
	s_add_i32 s6, s1, s5
	s_add_i32 s9, s6, 0x2000
	s_mov_b32 m0, s6
	s_waitcnt lgkmcnt(3)
	v_mfma_f32_16x16x32_bf16 v[160:163], v[164:167], v[180:183], v[160:163]
	s_add_i32 s8, s6, 0x4000
	s_add_i32 s7, s6, 0x6000
	v_mfma_f32_16x16x32_bf16 v[156:159], v[168:171], v[180:183], v[156:159]
	v_mfma_f32_16x16x32_bf16 v[152:155], v[172:175], v[180:183], v[152:155]
	v_mfma_f32_16x16x32_bf16 v[148:151], v[176:179], v[180:183], v[148:151]
	s_waitcnt lgkmcnt(2)
	v_mfma_f32_16x16x32_bf16 v[144:147], v[164:167], v[184:187], v[144:147]
	v_mfma_f32_16x16x32_bf16 v[140:143], v[168:171], v[184:187], v[140:143]
	v_mfma_f32_16x16x32_bf16 v[136:139], v[172:175], v[184:187], v[136:139]
	v_mfma_f32_16x16x32_bf16 v[132:135], v[176:179], v[184:187], v[132:135]
	ds_read_b128 v[180:183], v208 offset:8192
	ds_read_b128 v[184:187], v208 offset:10240
	ds_read_b128 v[196:199], v208 offset:12288
	ds_read_b128 v[200:203], v208 offset:14336
	buffer_load_dwordx4 v225, s[36:39], s4 offen lds
	s_mov_b32 m0, s9
	s_waitcnt lgkmcnt(5)
	v_mfma_f32_16x16x32_bf16 v[128:131], v[164:167], v[188:191], v[128:131]
	buffer_load_dwordx4 v226, s[36:39], s4 offen lds
	s_mov_b32 m0, s8
	s_nop 0
	buffer_load_dwordx4 v224, s[36:39], s4 offen lds
	s_mov_b32 m0, s7
	v_mfma_f32_16x16x32_bf16 v[124:127], v[168:171], v[188:191], v[124:127]
	buffer_load_dwordx4 v223, s[36:39], s4 offen lds
	v_mfma_f32_16x16x32_bf16 v[120:123], v[172:175], v[188:191], v[120:123]
	v_mfma_f32_16x16x32_bf16 v[116:119], v[176:179], v[188:191], v[116:119]
	s_waitcnt lgkmcnt(4)
	v_mfma_f32_16x16x32_bf16 v[112:115], v[164:167], v[192:195], v[112:115]
	v_mfma_f32_16x16x32_bf16 v[108:111], v[168:171], v[192:195], v[108:111]
	v_mfma_f32_16x16x32_bf16 v[104:107], v[172:175], v[192:195], v[104:107]
	v_mfma_f32_16x16x32_bf16 v[100:103], v[176:179], v[192:195], v[100:103]
	s_cmp_eq_u32 s98, 0
	s_cbranch_scc1 .Lmy_elda
	s_waitcnt lgkmcnt(3)
	v_mfma_f32_16x16x32_bf16 v[96:99], v[164:167], v[180:183], v[96:99]
	v_mfma_f32_16x16x32_bf16 v[92:95], v[168:171], v[180:183], v[92:95]
	v_mfma_f32_16x16x32_bf16 v[88:91], v[172:175], v[180:183], v[88:91]
	v_mfma_f32_16x16x32_bf16 v[84:87], v[176:179], v[180:183], v[84:87]
	s_waitcnt lgkmcnt(2)
	v_mfma_f32_16x16x32_bf16 v[80:83], v[164:167], v[184:187], v[80:83]
	v_mfma_f32_16x16x32_bf16 v[76:79], v[168:171], v[184:187], v[76:79]
	v_mfma_f32_16x16x32_bf16 v[72:75], v[172:175], v[184:187], v[72:75]
	v_mfma_f32_16x16x32_bf16 v[68:71], v[176:179], v[184:187], v[68:71]
	s_cmp_lt_u32 s98, 2
	s_cbranch_scc1 .Lmy_elda
	s_waitcnt lgkmcnt(1)
	v_mfma_f32_16x16x32_bf16 v[64:67], v[164:167], v[196:199], v[64:67]
	v_mfma_f32_16x16x32_bf16 v[60:63], v[168:171], v[196:199], v[60:63]
	v_mfma_f32_16x16x32_bf16 v[56:59], v[172:175], v[196:199], v[56:59]
	v_mfma_f32_16x16x32_bf16 v[52:55], v[176:179], v[196:199], v[52:55]
	s_waitcnt lgkmcnt(0)
	v_mfma_f32_16x16x32_bf16 v[48:51], v[164:167], v[200:203], v[48:51]
	v_mfma_f32_16x16x32_bf16 v[44:47], v[168:171], v[200:203], v[44:47]

; #define G_DMA_A(buf, t, i_) __builtin_amdgcn_raw_ptr_buffer_load_lds(ra, (LAS void*)(lds + (buf) * 65536 + a_wu + (i_) * 8192), 16, ao##i_, (unsigned)(t) * 128u, 0, 0)
; #define G_ISSUE_B(t) do { const unsigned so_ = (unsigned)(t) * 64u * ldbB; _Pragma("unroll") for (int i_ = 0; i_ < 8; ++i_) sb[i_] = __builtin_bit_cast(f32x4, __builtin_amdgcn_raw_buffer_load_b128(rb, bo, so_ + (unsigned)i_ * ldbB, 0)); } while (0)
; #define G_RETIRE() asm volatile("s_waitcnt vmcnt(0)" : "+v"(sb[0]), "+v"(sb[1]), "+v"(sb[2]), "+v"(sb[3]), "+v"(sb[4]), "+v"(sb[5]), "+v"(sb[6]), "+v"(sb[7]) :: "memory")
; #define G_WRITE_B(buf) do { LAS unsigned char* d_ = lds + (buf) * 65536; \
;         _Pragma("unroll") for (int j_ = 0; j_ < 4; ++j_) { u32x4 w_; w_.x = cvtpk(sb[0][j_], sb[1][j_]); w_.y = cvtpk(sb[2][j_], sb[3][j_]); w_.z = cvtpk(sb[4][j_], sb[5][j_]); w_.w = cvtpk(sb[6][j_], sb[7][j_]); \
;             *(LAS u32x4*)(d_ + 32768 + T.b_w + ((T.b_rot + 64u * j_) & 255u)) = w_; } } while (0)
; #define G_LDB(dst, buf, ks) do { const LAS unsigned char* s_ = lds + (buf) * 65536 + (ks) * 1024; _Pragma("unroll") for (int n_ = 0; n_ < 4; ++n_) dst[n_] = *(const LAS bf16x8*)(s_ + T.b_r + n_ * 2048); } while (0)
; #define G_LDA(dst, buf, ks, h_) do { const LAS unsigned char* s_ = lds + (buf) * 65536 + (ks) * 1024; _Pragma("unroll") for (int m_ = 0; m_ < 4; ++m_) dst[m_] = *(const LAS bf16x8*)(s_ + T.a_r + ((h_) * 4 + m_) * 2048); } while (0)
; #define G_SB() __builtin_amdgcn_sched_barrier(0)
; #define G_BAR() do { asm volatile("s_waitcnt lgkmcnt(0)" ::: "memory"); __builtin_amdgcn_s_barrier(); asm volatile("" ::: "memory"); } while (0)
; __device__ __forceinline__ void gemm_kloop(f32x4 (&acc)[8][4], LAS unsigned char* lds, const GemmT& T, ...
;     ...
;     for (int t = 0; t < nt; ++t) { const int cur = t & 1; const bool w1 = t + 1 < nt, i2 = t + 2 < nt;
;         G_LDB(Bf0, cur, 0); G_LDA(AtA, cur, 0, 0); G_SB();
;         G_LDA(AtB, cur, 0, 1); if (w1) { G_DMA_A(cur ^ 1, t + 1, 0); G_DMA_A(cur ^ 1, t + 1, 1); G_DMA_A(cur ^ 1, t + 1, 2); G_DMA_A(cur ^ 1, t + 1, 3); } G_MMA(AtA, Bf0, 0); G_SB();
;         G_LDB(Bf1, cur, 1); G_LDA(AtA, cur, 1, 0); G_MMA(AtB, Bf0, 1); G_SB();
;         G_LDA(AtB, cur, 1, 1); if (w1) { G_RETIRE(); G_WRITE_B(cur ^ 1); } if (i2) G_ISSUE_B(t + 2); G_MMA(AtA, Bf1, 0); G_SB();
;         G_MMA(AtB, Bf1, 1); G_SB();
;         G_BAR(); }
.Lmy_eldc:
	s_waitcnt vmcnt(0)
	s_add_i32 s6, s3, 0xffff2000
	s_waitcnt lgkmcnt(3)
	v_mfma_f32_16x16x32_bf16 v[160:163], v[164:167], v[176:179], v[160:163]
	v_cvt_pk_bf16_f32 v230, v5, v9
	v_cvt_pk_bf16_f32 v234, v6, v10
	s_add_i32 s7, s3, 0xffff4000
	v_mfma_f32_16x16x32_bf16 v[156:159], v[168:171], v[176:179], v[156:159]
	v_cvt_pk_bf16_f32 v231, v13, v17
	v_cvt_pk_bf16_f32 v235, v14, v18
	v_cvt_pk_bf16_f32 v232, v21, v29
	v_mfma_f32_16x16x32_bf16 v[152:155], v[180:183], v[176:179], v[152:155]
	v_cvt_pk_bf16_f32 v236, v22, v30
	v_cvt_pk_bf16_f32 v233, v25, v33
	v_cvt_pk_bf16_f32 v237, v26, v34
	v_mfma_f32_16x16x32_bf16 v[148:151], v[184:187], v[176:179], v[148:151]
	v_cvt_pk_bf16_f32 v172, v4, v8
	v_cvt_pk_bf16_f32 v173, v12, v16
	v_cvt_pk_bf16_f32 v174, v20, v28
	s_waitcnt lgkmcnt(2)
	v_mfma_f32_16x16x32_bf16 v[144:147], v[164:167], v[200:203], v[144:147]
	v_cvt_pk_bf16_f32 v175, v24, v32
	v_add_u32_e32 v3, s5, v228
	v_mfma_f32_16x16x32_bf16 v[140:143], v[168:171], v[200:203], v[140:143]
	v_mfma_f32_16x16x32_bf16 v[136:139], v[180:183], v[200:203], v[136:139]
	v_mfma_f32_16x16x32_bf16 v[132:135], v[184:187], v[200:203], v[132:135]
	v_cvt_pk_bf16_f32 v188, v7, v11
	buffer_load_dwordx4 v[4:7], v222, s[24:27], s6 offen
	buffer_load_dwordx4 v[8:11], v222, s[24:27], s7 offen
	s_add_i32 s6, s3, 0xffff6000
	v_cvt_pk_bf16_f32 v189, v15, v19
	s_add_i32 s7, s3, 0xffff8000
	buffer_load_dwordx4 v[12:15], v222, s[24:27], s6 offen
	buffer_load_dwordx4 v[16:19], v222, s[24:27], s7 offen
	s_add_i32 s6, s3, 0xffffa000
	v_cvt_pk_bf16_f32 v190, v23, v31
	s_add_i32 s7, s3, 0xffffc000
	buffer_load_dwordx4 v[20:23], v222, s[24:27], s6 offen
	buffer_load_dwordx4 v[28:31], v222, s[24:27], s7 offen
	s_add_i32 s6, s3, 0xffffe000
	v_cvt_pk_bf16_f32 v191, v27, v35
	buffer_load_dwordx4 v[24:27], v222, s[24:27], s6 offen
	buffer_load_dwordx4 v[32:35], v222, s[24:27], s3 offen
	s_waitcnt lgkmcnt(1)
	v_mfma_f32_16x16x32_bf16 v[128:131], v[164:167], v[204:207], v[128:131]
	v_mfma_f32_16x16x32_bf16 v[124:127], v[168:171], v[204:207], v[124:127]
	v_mfma_f32_16x16x32_bf16 v[120:123], v[180:183], v[204:207], v[120:123]
	v_mfma_f32_16x16x32_bf16 v[116:119], v[184:187], v[204:207], v[116:119]
	v_add_u32_e32 v192, v3, v219
	v_add_u32_e32 v3, v3, v221
	ds_write_b128 v192, v[172:175] offset:32768
	ds_write_b128 v192, v[230:233] offset:32832
	s_waitcnt lgkmcnt(2)
	v_mfma_f32_16x16x32_bf16 v[112:115], v[164:167], v[208:211], v[112:115]
	ds_write_b128 v192, v[234:237] offset:32896
	ds_write_b128 v3, v[188:191] offset:32768
	v_mfma_f32_16x16x32_bf16 v[108:111], v[168:171], v[208:211], v[108:111]
	v_mfma_f32_16x16x32_bf16 v[104:107], v[180:183], v[208:211], v[104:107]
	v_mfma_f32_16x16x32_bf16 v[100:103], v[184:187], v[208:211], v[100:103]
	s_waitcnt lgkmcnt(0)
	s_barrier
	s_add_i32 s3, s3, 0x80000
	s_addk_i32 s4, 0x80
	s_add_i32 s2, s2, 0x10000
	s_cmp_lg_u32 s3, 0x100e000
	s_cbranch_scc1 .LBB0_1576
	v_add_u32_e32 v3, 0, v227
	v_add_u32_e32 v204, 0, v217
	ds_read_b128 v[164:167], v3 offset:32768
	ds_read_b128 v[168:171], v3 offset:34816
	ds_read_b128 v[172:175], v3 offset:36864
	ds_read_b128 v[176:179], v3 offset:38912
	ds_read_b128 v[180:183], v204
	ds_read_b128 v[184:187], v204 offset:2048
	ds_read_b128 v[188:191], v204 offset:4096
	ds_read_b128 v[192:195], v204 offset:6144
	s_add_i32 m0, s1, 0x10000
	s_add_i32 s2, s1, 0x16000
	s_add_i32 s3, s1, 0x14000
	s_add_i32 s1, s1, 0x12000
	s_mov_b32 s38, s26
	s_mov_b32 s39, s27
	s_waitcnt lgkmcnt(3)
	v_mfma_f32_16x16x32_bf16 v[160:163], v[164:167], v[180:183], v[160:163]
	v_mfma_f32_16x16x32_bf16 v[156:159], v[168:171], v[180:183], v[156:159]
	v_mfma_f32_16x16x32_bf16 v[152:155], v[172:175], v[180:183], v[152:155]
	v_mfma_f32_16x16x32_bf16 v[148:151], v[176:179], v[180:183], v[148:151]
	s_waitcnt lgkmcnt(2)
	v_mfma_f32_16x16x32_bf16 v[144:147], v[164:167], v[184:187], v[144:147]
	v_mfma_f32_16x16x32_bf16 v[140:143], v[168:171], v[184:187], v[140:143]
	v_mfma_f32_16x16x32_bf16 v[136:139], v[172:175], v[184:187], v[136:139]
	v_mfma_f32_16x16x32_bf16 v[132:135], v[176:179], v[184:187], v[132:135]
	ds_read_b128 v[180:183], v204 offset:8192
	ds_read_b128 v[184:187], v204 offset:10240
	ds_read_b128 v[196:199], v204 offset:12288
	ds_read_b128 v[200:203], v204 offset:14336
	buffer_load_dwordx4 v225, s[36:39], s79 offen lds
	s_mov_b32 m0, s1
	s_waitcnt lgkmcnt(4)
	v_mfma_f32_16x16x32_bf16 v[108:111], v[168:171], v[192:195], v[108:111]
	buffer_load_dwordx4 v226, s[36:39], s79 offen lds
	s_mov_b32 m0, s3
	s_nop 0
	buffer_load_dwordx4 v224, s[36:39], s79 offen lds
	s_mov_b32 m0, s2
	v_mfma_f32_16x16x32_bf16 v[104:107], v[172:175], v[192:195], v[104:107]
	buffer_load_dwordx4 v223, s[36:39], s79 offen lds
	v_mfma_f32_16x16x32_bf16 v[100:103], v[176:179], v[192:195], v[100:103]
	v_mfma_f32_16x16x32_bf16 v[128:131], v[164:167], v[188:191], v[128:131]
	v_mfma_f32_16x16x32_bf16 v[124:127], v[168:171], v[188:191], v[124:127]
	v_mfma_f32_16x16x32_bf16 v[120:123], v[172:175], v[188:191], v[120:123]
	v_mfma_f32_16x16x32_bf16 v[116:119], v[176:179], v[188:191], v[116:119]
	v_mfma_f32_16x16x32_bf16 v[112:115], v[164:167], v[192:195], v[112:115]
	s_waitcnt lgkmcnt(3)
	v_mfma_f32_16x16x32_bf16 v[96:99], v[164:167], v[180:183], v[96:99]
	v_mfma_f32_16x16x32_bf16 v[92:95], v[168:171], v[180:183], v[92:95]
	v_mfma_f32_16x16x32_bf16 v[88:91], v[172:175], v[180:183], v[88:91]
	v_mfma_f32_16x16x32_bf16 v[84:87], v[176:179], v[180:183], v[84:87]
	s_waitcnt lgkmcnt(2)
	v_mfma_f32_16x16x32_bf16 v[80:83], v[164:167], v[184:187], v[80:83]
	v_mfma_f32_16x16x32_bf16 v[76:79], v[168:171], v[184:187], v[76:79]
	v_mfma_f32_16x16x32_bf16 v[72:75], v[172:175], v[184:187], v[72:75]
	v_mfma_f32_16x16x32_bf16 v[68:71], v[176:179], v[184:187], v[68:71]
	s_waitcnt lgkmcnt(1)
; #define G_DMA_A(buf, t, i_) __builtin_amdgcn_raw_ptr_buffer_load_lds(ra, (LAS void*)(lds + (buf) * 65536 + a_wu + (i_) * 8192), 16, ao##i_, (unsigned)(t) * 128u, 0, 0)
; #define G_ISSUE_B(t) do { const unsigned so_ = (unsigned)(t) * 64u * ldbB; _Pragma("unroll") for (int i_ = 0; i_ < 8; ++i_) sb[i_] = __builtin_bit_cast(f32x4, __builtin_amdgcn_raw_buffer_load_b128(rb, bo, so_ + (unsigned)i_ * ldbB, 0)); } while (0)
; #define G_RETIRE() asm volatile("s_waitcnt vmcnt(0)" : "+v"(sb[0]), "+v"(sb[1]), "+v"(sb[2]), "+v"(sb[3]), "+v"(sb[4]), "+v"(sb[5]), "+v"(sb[6]), "+v"(sb[7]) :: "memory")
; #define G_WRITE_B(buf) do { LAS unsigned char* d_ = lds + (buf) * 65536; \
;         _Pragma("unroll") for (int j_ = 0; j_ < 4; ++j_) { u32x4 w_; w_.x = cvtpk(sb[0][j_], sb[1][j_]); w_.y = cvtpk(sb[2][j_], sb[3][j_]); w_.z = cvtpk(sb[4][j_], sb[5][j_]); w_.w = cvtpk(sb[6][j_], sb[7][j_]); \
;             *(LAS u32x4*)(d_ + 32768 + T.b_w + ((T.b_rot + 64u * j_) & 255u)) = w_; } } while (0)
; #define G_LDB(dst, buf, ks) do { const LAS unsigned char* s_ = lds + (buf) * 65536 + (ks) * 1024; _Pragma("unroll") for (int n_ = 0; n_ < 4; ++n_) dst[n_] = *(const LAS bf16x8*)(s_ + T.b_r + n_ * 2048); } while (0)
; #define G_LDA(dst, buf, ks, h_) do { const LAS unsigned char* s_ = lds + (buf) * 65536 + (ks) * 1024; _Pragma("unroll") for (int m_ = 0; m_ < 4; ++m_) dst[m_] = *(const LAS bf16x8*)(s_ + T.a_r + ((h_) * 4 + m_) * 2048); } while (0)
; #define G_SB() __builtin_amdgcn_sched_barrier(0)
; #define G_BAR() do { asm volatile("s_waitcnt lgkmcnt(0)" ::: "memory"); __builtin_amdgcn_s_barrier(); asm volatile("" ::: "memory"); } while (0)
; __device__ __forceinline__ void gemm_kloop(f32x4 (&acc)[8][4], LAS unsigned char* lds, const GemmT& T, ...
;     ...
;     for (int t = 0; t < nt; ++t) { const int cur = t & 1; const bool w1 = t + 1 < nt, i2 = t + 2 < nt;
;         G_LDB(Bf0, cur, 0); G_LDA(AtA, cur, 0, 0); G_SB();
;         G_LDA(AtB, cur, 0, 1); if (w1) { G_DMA_A(cur ^ 1, t + 1, 0); G_DMA_A(cur ^ 1, t + 1, 1); G_DMA_A(cur ^ 1, t + 1, 2); G_DMA_A(cur ^ 1, t + 1, 3); } G_MMA(AtA, Bf0, 0); G_SB();
;         G_LDB(Bf1, cur, 1); G_LDA(AtA, cur, 1, 0); G_MMA(AtB, Bf0, 1); G_SB();
;         G_LDA(AtB, cur, 1, 1); if (w1) { G_RETIRE(); G_WRITE_B(cur ^ 1); } if (i2) G_ISSUE_B(t + 2); G_MMA(AtA, Bf1, 0); G_SB();
;         G_MMA(AtB, Bf1, 1); G_SB();
;         G_BAR(); }
	v_mfma_f32_16x16x32_bf16 v[64:67], v[164:167], v[196:199], v[64:67]
	v_mfma_f32_16x16x32_bf16 v[60:63], v[168:171], v[196:199], v[60:63]
	v_mfma_f32_16x16x32_bf16 v[56:59], v[172:175], v[196:199], v[56:59]
	v_mfma_f32_16x16x32_bf16 v[52:55], v[176:179], v[196:199], v[52:55]
	s_waitcnt lgkmcnt(0)
	v_mfma_f32_16x16x32_bf16 v[48:51], v[164:167], v[200:203], v[48:51]
	v_mfma_f32_16x16x32_bf16 v[44:47], v[168:171], v[200:203], v[44:47]
	ds_read_b128 v[164:167], v3 offset:33792
	ds_read_b128 v[168:171], v3 offset:35840
	ds_read_b128 v[180:183], v3 offset:37888
	ds_read_b128 v[184:187], v3 offset:39936
	v_mfma_f32_16x16x32_bf16 v[40:43], v[172:175], v[200:203], v[40:43]
	ds_read_b128 v[172:175], v204 offset:1024
	ds_read_b128 v[188:191], v204 offset:3072
	ds_read_b128 v[192:195], v204 offset:5120
	ds_read_b128 v[196:199], v204 offset:7168
	v_mfma_f32_16x16x32_bf16 v[36:39], v[176:179], v[200:203], v[36:39]
	s_waitcnt lgkmcnt(3)
	v_mfma_f32_16x16x32_bf16 v[160:163], v[164:167], v[172:175], v[160:163]
	v_add_u32_e32 v3, s29, v220
	v_mfma_f32_16x16x32_bf16 v[156:159], v[168:171], v[172:175], v[156:159]
	v_mfma_f32_16x16x32_bf16 v[152:155], v[180:183], v[172:175], v[152:155]
	v_mfma_f32_16x16x32_bf16 v[148:151], v[184:187], v[172:175], v[148:151]
	ds_read_b128 v[172:175], v204 offset:9216
	ds_read_b128 v[176:179], v204 offset:11264
	ds_read_b128 v[200:203], v204 offset:13312
	ds_read_b128 v[204:207], v204 offset:15360
	s_waitcnt vmcnt(4)
	s_waitcnt vmcnt(0)
	s_waitcnt lgkmcnt(6)
	v_mfma_f32_16x16x32_bf16 v[144:147], v[164:167], v[188:191], v[144:147]
	v_mfma_f32_16x16x32_bf16 v[140:143], v[168:171], v[188:191], v[140:143]
	v_mfma_f32_16x16x32_bf16 v[136:139], v[180:183], v[188:191], v[136:139]
	v_mfma_f32_16x16x32_bf16 v[132:135], v[184:187], v[188:191], v[132:135]
	v_cvt_pk_bf16_f32 v188, v4, v8
	v_cvt_pk_bf16_f32 v189, v12, v16
	v_cvt_pk_bf16_f32 v190, v20, v28
	v_cvt_pk_bf16_f32 v191, v24, v32
	v_add_u32_e32 v4, v3, v219
	ds_write_b128 v4, v[188:191]
	v_cvt_pk_bf16_f32 v188, v5, v9
	v_cvt_pk_bf16_f32 v189, v13, v17
	v_cvt_pk_bf16_f32 v190, v21, v29
	v_cvt_pk_bf16_f32 v191, v25, v33
	ds_write_b128 v4, v[188:191] offset:64
	v_cvt_pk_bf16_f32 v188, v6, v10
	v_cvt_pk_bf16_f32 v189, v14, v18
	v_cvt_pk_bf16_f32 v190, v22, v30
	v_cvt_pk_bf16_f32 v191, v26, v34
	ds_write_b128 v4, v[188:191] offset:128
	v_cvt_pk_bf16_f32 v4, v7, v11
	v_cvt_pk_bf16_f32 v5, v15, v19
	v_cvt_pk_bf16_f32 v6, v23, v31
	v_cvt_pk_bf16_f32 v7, v27, v35
	v_add_u32_e32 v3, v3, v221
	s_waitcnt lgkmcnt(7)
	v_mfma_f32_16x16x32_bf16 v[108:111], v[168:171], v[196:199], v[108:111]
	ds_write_b128 v3, v[4:7]
	v_mfma_f32_16x16x32_bf16 v[8:11], v[180:183], v[196:199], v[104:107]
	v_mfma_f32_16x16x32_bf16 v[4:7], v[184:187], v[196:199], v[100:103]
	v_mfma_f32_16x16x32_bf16 v[128:131], v[164:167], v[192:195], v[128:131]
	v_mfma_f32_16x16x32_bf16 v[124:127], v[168:171], v[192:195], v[124:127]
	v_mfma_f32_16x16x32_bf16 v[120:123], v[180:183], v[192:195], v[120:123]
	v_mfma_f32_16x16x32_bf16 v[116:119], v[184:187], v[192:195], v[116:119]
	v_mfma_f32_16x16x32_bf16 v[112:115], v[164:167], v[196:199], v[112:115]
	s_waitcnt lgkmcnt(7)
	v_mfma_f32_16x16x32_bf16 v[12:15], v[164:167], v[172:175], v[96:99]
	v_mfma_f32_16x16x32_bf16 v[16:19], v[168:171], v[172:175], v[92:95]
	v_mfma_f32_16x16x32_bf16 v[20:23], v[180:183], v[172:175], v[88:91]
	v_mfma_f32_16x16x32_bf16 v[24:27], v[184:187], v[172:175], v[84:87]
	s_waitcnt lgkmcnt(6)
	v_mfma_f32_16x16x32_bf16 v[28:31], v[164:167], v[176:179], v[80:83]
	v_mfma_f32_16x16x32_bf16 v[32:35], v[168:171], v[176:179], v[76:79]
	v_mfma_f32_16x16x32_bf16 v[72:75], v[180:183], v[176:179], v[72:75]
	v_mfma_f32_16x16x32_bf16 v[68:71], v[184:187], v[176:179], v[68:71]
	s_waitcnt lgkmcnt(5)
	v_mfma_f32_16x16x32_bf16 v[64:67], v[164:167], v[200:203], v[64:67]
	v_mfma_f32_16x16x32_bf16 v[60:63], v[168:171], v[200:203], v[60:63]
	v_mfma_f32_16x16x32_bf16 v[56:59], v[180:183], v[200:203], v[56:59]
	v_mfma_f32_16x16x32_bf16 v[52:55], v[184:187], v[200:203], v[52:55]
	s_waitcnt lgkmcnt(4)
	v_mfma_f32_16x16x32_bf16 v[48:51], v[164:167], v[204:207], v[48:51]
	v_mfma_f32_16x16x32_bf16 v[44:47], v[168:171], v[204:207], v[44:47]
	v_mfma_f32_16x16x32_bf16 v[40:43], v[180:183], v[204:207], v[40:43]
	v_mfma_f32_16x16x32_bf16 v[36:39], v[184:187], v[204:207], v[36:39]
	s_add_i32 s1, 0, 0x10000
	s_waitcnt lgkmcnt(0)
	s_barrier
; #define G_DMA_A(buf, t, i_) __builtin_amdgcn_raw_ptr_buffer_load_lds(ra, (LAS void*)(lds + (buf) * 65536 + a_wu + (i_) * 8192), 16, ao##i_, (unsigned)(t) * 128u, 0, 0)
; #define G_ISSUE_B(t) do { const unsigned so_ = (unsigned)(t) * 64u * ldbB; _Pragma("unroll") for (int i_ = 0; i_ < 8; ++i_) sb[i_] = __builtin_bit_cast(f32x4, __builtin_amdgcn_raw_buffer_load_b128(rb, bo, so_ + (unsigned)i_ * ldbB, 0)); } while (0)
; #define G_RETIRE() asm volatile("s_waitcnt vmcnt(0)" : "+v"(sb[0]), "+v"(sb[1]), "+v"(sb[2]), "+v"(sb[3]), "+v"(sb[4]), "+v"(sb[5]), "+v"(sb[6]), "+v"(sb[7]) :: "memory")
; #define G_WRITE_B(buf) do { LAS unsigned char* d_ = lds + (buf) * 65536; \
;         _Pragma("unroll") for (int j_ = 0; j_ < 4; ++j_) { u32x4 w_; w_.x = cvtpk(sb[0][j_], sb[1][j_]); w_.y = cvtpk(sb[2][j_], sb[3][j_]); w_.z = cvtpk(sb[4][j_], sb[5][j_]); w_.w = cvtpk(sb[6][j_], sb[7][j_]); \
;             *(LAS u32x4*)(d_ + 32768 + T.b_w + ((T.b_rot + 64u * j_) & 255u)) = w_; } } while (0)
; #define G_LDB(dst, buf, ks) do { const LAS unsigned char* s_ = lds + (buf) * 65536 + (ks) * 1024; _Pragma("unroll") for (int n_ = 0; n_ < 4; ++n_) dst[n_] = *(const LAS bf16x8*)(s_ + T.b_r + n_ * 2048); } while (0)
; #define G_LDA(dst, buf, ks, h_) do { const LAS unsigned char* s_ = lds + (buf) * 65536 + (ks) * 1024; _Pragma("unroll") for (int m_ = 0; m_ < 4; ++m_) dst[m_] = *(const LAS bf16x8*)(s_ + T.a_r + ((h_) * 4 + m_) * 2048); } while (0)
; #define G_SB() __builtin_amdgcn_sched_barrier(0)
; #define G_BAR() do { asm volatile("s_waitcnt lgkmcnt(0)" ::: "memory"); __builtin_amdgcn_s_barrier(); asm volatile("" ::: "memory"); } while (0)
; __device__ __forceinline__ void gemm_kloop(f32x4 (&acc)[8][4], LAS unsigned char* lds, const GemmT& T, ...
;     ...
;     for (int t = 0; t < nt; ++t) { const int cur = t & 1; const bool w1 = t + 1 < nt, i2 = t + 2 < nt;
;         G_LDB(Bf0, cur, 0); G_LDA(AtA, cur, 0, 0); G_SB();
;         G_LDA(AtB, cur, 0, 1); if (w1) { G_DMA_A(cur ^ 1, t + 1, 0); G_DMA_A(cur ^ 1, t + 1, 1); G_DMA_A(cur ^ 1, t + 1, 2); G_DMA_A(cur ^ 1, t + 1, 3); } G_MMA(AtA, Bf0, 0); G_SB();
;         G_LDB(Bf1, cur, 1); G_LDA(AtA, cur, 1, 0); G_MMA(AtB, Bf0, 1); G_SB();
;         G_LDA(AtB, cur, 1, 1); if (w1) { G_RETIRE(); G_WRITE_B(cur ^ 1); } if (i2) G_ISSUE_B(t + 2); G_MMA(AtA, Bf1, 0); G_SB();
;         G_MMA(AtB, Bf1, 1); G_SB();
;         G_BAR(); }
	v_add_u32_e32 v3, s1, v218
	ds_read_b128 v[76:79], v3
	ds_read_b128 v[80:83], v3 offset:2048
	ds_read_b128 v[84:87], v3 offset:4096
	ds_read_b128 v[88:91], v3 offset:6144
	v_add_u32_e32 v3, s1, v217
	ds_read_b128 v[92:95], v3
	ds_read_b128 v[96:99], v3 offset:2048
	ds_read_b128 v[100:103], v3 offset:4096
	ds_read_b128 v[104:107], v3 offset:6144
	s_waitcnt lgkmcnt(2)
	v_mfma_f32_16x16x32_bf16 v[144:147], v[76:79], v[96:99], v[144:147]
	v_mfma_f32_16x16x32_bf16 v[140:143], v[80:83], v[96:99], v[140:143]
	v_mfma_f32_16x16x32_bf16 v[170:173], v[84:87], v[96:99], v[136:139]
	v_mfma_f32_16x16x32_bf16 v[96:99], v[88:91], v[96:99], v[132:135]
	s_waitcnt lgkmcnt(1)
	v_mfma_f32_16x16x32_bf16 v[128:131], v[76:79], v[100:103], v[128:131]
	v_mfma_f32_16x16x32_bf16 v[124:127], v[80:83], v[100:103], v[124:127]
	v_mfma_f32_16x16x32_bf16 v[120:123], v[84:87], v[100:103], v[120:123]
	v_mfma_f32_16x16x32_bf16 v[116:119], v[88:91], v[100:103], v[116:119]
	s_waitcnt lgkmcnt(0)
	v_mfma_f32_16x16x32_bf16 v[174:177], v[80:83], v[104:107], v[108:111]
	ds_read_b128 v[100:103], v3 offset:8192
	s_nop 1
	ds_read_b128 v[108:111], v3 offset:10240
	ds_read_b128 v[132:135], v3 offset:12288
	ds_read_b128 v[136:139], v3 offset:14336
	v_mfma_f32_16x16x32_bf16 v[160:163], v[76:79], v[92:95], v[160:163]
	v_mfma_f32_16x16x32_bf16 v[164:167], v[80:83], v[92:95], v[156:159]
	v_mfma_f32_16x16x32_bf16 v[152:155], v[84:87], v[92:95], v[152:155]
	v_mfma_f32_16x16x32_bf16 v[92:95], v[88:91], v[92:95], v[148:151]
	v_mfma_f32_16x16x32_bf16 v[8:11], v[84:87], v[104:107], v[8:11]
	v_mfma_f32_16x16x32_bf16 v[4:7], v[88:91], v[104:107], v[4:7]
	v_mfma_f32_16x16x32_bf16 v[112:115], v[76:79], v[104:107], v[112:115]
	v_add_u32_e32 v3, s64, v218
	ds_read_b128 v[206:209], v3
	ds_read_b128 v[210:213], v3 offset:2048
	ds_read_b128 v[222:225], v3 offset:4096
	ds_read_b128 v[226:229], v3 offset:6144
	v_add_u32_e32 v3, s64, v217
	s_waitcnt lgkmcnt(5)
	v_mfma_f32_16x16x32_bf16 v[198:201], v[88:91], v[132:135], v[52:55]
	s_waitcnt lgkmcnt(4)
	v_mfma_f32_16x16x32_bf16 v[202:205], v[76:79], v[136:139], v[48:51]
	v_mfma_f32_16x16x32_bf16 v[218:221], v[80:83], v[136:139], v[44:47]
	v_mfma_f32_16x16x32_bf16 v[230:233], v[84:87], v[136:139], v[40:43]
	s_nop 2
	ds_read_b128 v[40:43], v3
	ds_read_b128 v[44:47], v3 offset:2048
	ds_read_b128 v[48:51], v3 offset:4096
	ds_read_b128 v[52:55], v3 offset:6144
	v_mfma_f32_16x16x32_bf16 v[12:15], v[76:79], v[100:103], v[12:15]
	v_mfma_f32_16x16x32_bf16 v[16:19], v[80:83], v[100:103], v[16:19]
	v_mfma_f32_16x16x32_bf16 v[20:23], v[84:87], v[100:103], v[20:23]
	v_mfma_f32_16x16x32_bf16 v[24:27], v[88:91], v[100:103], v[24:27]
	v_mfma_f32_16x16x32_bf16 v[28:31], v[76:79], v[108:111], v[28:31]
	v_mfma_f32_16x16x32_bf16 v[32:35], v[80:83], v[108:111], v[32:35]
	v_mfma_f32_16x16x32_bf16 v[178:181], v[84:87], v[108:111], v[72:75]
	v_mfma_f32_16x16x32_bf16 v[182:185], v[88:91], v[108:111], v[68:71]
	v_mfma_f32_16x16x32_bf16 v[186:189], v[76:79], v[132:135], v[64:67]
	v_mfma_f32_16x16x32_bf16 v[190:193], v[80:83], v[132:135], v[60:63]
	v_mfma_f32_16x16x32_bf16 v[194:197], v[84:87], v[132:135], v[56:59]
	v_mfma_f32_16x16x32_bf16 v[234:237], v[88:91], v[136:139], v[36:39]
	s_waitcnt lgkmcnt(3)
	v_mfma_f32_16x16x32_bf16 v[158:161], v[206:209], v[40:43], v[160:163]
	v_mfma_f32_16x16x32_bf16 v[166:169], v[210:213], v[40:43], v[164:167]
	v_mfma_f32_16x16x32_bf16 v[150:153], v[222:225], v[40:43], v[152:155]
	v_mfma_f32_16x16x32_bf16 v[154:157], v[226:229], v[40:43], v[92:95]
	s_waitcnt lgkmcnt(2)
	v_mfma_f32_16x16x32_bf16 v[134:137], v[206:209], v[44:47], v[144:147]
	v_mfma_f32_16x16x32_bf16 v[146:149], v[210:213], v[44:47], v[140:143]
	v_mfma_f32_16x16x32_bf16 v[102:105], v[222:225], v[44:47], v[170:173]
	v_mfma_f32_16x16x32_bf16 v[106:109], v[226:229], v[44:47], v[96:99]
	s_waitcnt lgkmcnt(1)
	v_mfma_f32_16x16x32_bf16 v[90:93], v[226:229], v[48:51], v[116:119]
	s_waitcnt lgkmcnt(0)
	v_mfma_f32_16x16x32_bf16 v[78:81], v[206:209], v[52:55], v[112:115]
	v_mfma_f32_16x16x32_bf16 v[70:73], v[222:225], v[52:55], v[8:11]
	s_nop 2
	ds_read_b128 v[8:11], v3 offset:8192
	ds_read_b128 v[42:45], v3 offset:10240
	ds_read_b128 v[110:113], v3 offset:12288
	ds_read_b128 v[114:117], v3 offset:14336
	v_mfma_f32_16x16x32_bf16 v[94:97], v[206:209], v[48:51], v[128:131]
	v_mfma_f32_16x16x32_bf16 v[98:101], v[210:213], v[48:51], v[124:127]
	v_mfma_f32_16x16x32_bf16 v[86:89], v[222:225], v[48:51], v[120:123]
	v_mfma_f32_16x16x32_bf16 v[82:85], v[210:213], v[52:55], v[174:177]
	v_mfma_f32_16x16x32_bf16 v[74:77], v[226:229], v[52:55], v[4:7]
	s_waitcnt lgkmcnt(3)
	v_mfma_f32_16x16x32_bf16 v[62:65], v[206:209], v[8:11], v[12:15]
	v_mfma_f32_16x16x32_bf16 v[66:69], v[210:213], v[8:11], v[16:19]
	v_mfma_f32_16x16x32_bf16 v[54:57], v[222:225], v[8:11], v[20:23]
	v_mfma_f32_16x16x32_bf16 v[58:61], v[226:229], v[8:11], v[24:27]
	s_waitcnt lgkmcnt(2)
	v_mfma_f32_16x16x32_bf16 v[46:49], v[206:209], v[42:45], v[28:31]
	v_mfma_f32_16x16x32_bf16 v[50:53], v[210:213], v[42:45], v[32:35]
	v_mfma_f32_16x16x32_bf16 v[38:41], v[222:225], v[42:45], v[178:181]
	v_mfma_f32_16x16x32_bf16 v[42:45], v[226:229], v[42:45], v[182:185]
	s_waitcnt lgkmcnt(1)
	v_mfma_f32_16x16x32_bf16 v[30:33], v[206:209], v[110:113], v[186:189]
	v_mfma_f32_16x16x32_bf16 v[34:37], v[210:213], v[110:113], v[190:193]
	v_mfma_f32_16x16x32_bf16 v[22:25], v[222:225], v[110:113], v[194:197]
	v_mfma_f32_16x16x32_bf16 v[26:29], v[226:229], v[110:113], v[198:201]
	s_waitcnt lgkmcnt(0)
	v_mfma_f32_16x16x32_bf16 v[14:17], v[206:209], v[114:117], v[202:205]
	v_mfma_f32_16x16x32_bf16 v[18:21], v[210:213], v[114:117], v[218:221]
	v_mfma_f32_16x16x32_bf16 v[6:9], v[222:225], v[114:117], v[230:233]
	v_mfma_f32_16x16x32_bf16 v[10:13], v[226:229], v[114:117], v[234:237]
	s_waitcnt lgkmcnt(0)
	s_barrier
